# GEMM unit-loop vmcnt0 hoisted to preheader; attention softmax chunks interleaved with PV MFMAs; attention prologue vmcnt3
# speedup vs baseline: 1.0031x; 1.0031x over previous
; #define PG8_STAGE(bufoff, gbase, voff) do { _Pragma("unroll") for (int _i = 0; _i < 2; ++_i) \
;         __builtin_amdgcn_global_load_lds((const __attribute__((address_space(1))) unsigned*)((const __attribute__((address_space(1))) char*)(gbase) + (unsigned)lnd_v((int)(voff)[_i])), (LAS unsigned*)(lds + (bufoff) + ldsw + _i * 8192), 16, 0, 0); } while (0)
; #define PG8_WAIT_V(n) asm volatile("s_waitcnt vmcnt(" #n ")" ::: "memory")
; #define PG8_BAR __builtin_amdgcn_s_barrier()
; template <class Desc, class Epi>
; __device__ __forceinline__ void gemm_phase(const int wv_, LAS unsigned char* lds, const Desc& d, const Epi& E) {
;     ...
;     const unsigned ldsw = (unsigned)wid * 1024u;
;     const int aoff = lds_byte(wr * 64 + fr, fq * 8), boff = lds_byte(wc * 32 + fr, fq * 8);
;     ...
;     const char* cA = (const char*)cur.a; const char* cB = (const char*)cur.b;
;     PG8_STAGE(PG8_SB(0, 0), cB, voffB); PG8_STAGE(PG8_SB(0, 1), cB + hstepB, voffB); PG8_STAGE(PG8_SA(0, 0), cA, voffA); PG8_STAGE(PG8_SA(0, 1), cA, voffA1);
;     if (wr == 1) PG8_BAR;
;     PG8_WAIT_V(2); PG8_BAR;
;     PG8_STAGE(PG8_SB(1, 0), cB + kstep, voffB); PG8_STAGE(PG8_SA(1, 0), cA + kstep, voffA); PG8_STAGE(PG8_SB(1, 1), cB + hstepB + kstep, voffB);
;     PG8_WAIT_V(6); PG8_BAR;
.LBB0_741:
	s_lshr_b32 s1, s1, 2
	v_mov_b32_e32 v96, v134
	s_add_u32 s38, s29, 0x43200000
	s_waitcnt vmcnt(2)
	s_barrier
	s_addc_u32 s39, s3, 0
	v_lshl_add_u64 v[0:1], s[4:5], 0, v[96:97]
	s_add_i32 m0, s55, 0x18000
	v_lshl_add_u64 v[0:1], v[0:1], 0, s[30:31]
	v_mov_b32_e32 v96, v137
	global_load_lds_dwordx4 v[0:1], off
	s_add_i32 m0, s55, 0x1a000
	v_lshl_add_u64 v[0:1], s[4:5], 0, v[96:97]
	v_lshl_add_u64 v[0:1], v[0:1], 0, s[30:31]
	v_mov_b32_e32 v96, v132
	global_load_lds_dwordx4 v[0:1], off
	s_add_i32 s59, s55, 0x8000
	v_lshl_add_u64 v[0:1], s[20:21], 0, v[96:97]
	s_lshl_b32 s29, s41, 5
	v_lshl_add_u64 v[0:1], v[0:1], 0, s[30:31]
	s_mov_b32 m0, s59
	v_mov_b32_e32 v96, v135
	s_and_b32 s29, s29, 0x60
	global_load_lds_dwordx4 v[0:1], off
	s_add_i32 s60, s55, 0xa000
	v_lshl_add_u64 v[0:1], s[20:21], 0, v[96:97]
	s_lshl_b32 s3, s40, 13
	s_lshl_b32 s41, s29, 7
	v_lshl_add_u64 v[0:1], v[0:1], 0, s[30:31]
	s_mov_b32 m0, s60
	s_add_u32 s42, s4, 0x40080
	global_load_lds_dwordx4 v[0:1], off
	v_mov_b32_e32 v0, v134
	s_addc_u32 s43, s5, 0
	s_add_i32 m0, s55, 0x1c000
	v_lshrrev_b32_e32 v1, 1, v4
	global_load_lds_dwordx4 v0, s[42:43]
	v_mov_b32_e32 v0, v137
	s_add_i32 m0, s55, 0x1e000
	v_and_b32_e32 v1, 24, v1
	global_load_lds_dwordx4 v0, s[42:43]
	v_and_b32_e32 v0, 15, v4
	v_lshl_or_b32 v138, s40, 6, v0
	v_lshlrev_b32_e32 v2, 1, v1
	v_lshl_or_b32 v0, v0, 6, v2
	v_lshlrev_b32_e32 v2, 2, v138
	v_lshlrev_b32_e32 v4, 2, v4
	v_and_b32_e32 v3, 32, v2
	v_and_b32_e32 v4, 32, v4
	s_waitcnt vmcnt(6)
	s_cmpk_lt_u32 s2, 0x100
	v_bitop3_b32 v3, v0, s3, v3 bitop3:0xde
	v_bitop3_b32 v139, v0, s41, v4 bitop3:0xde
	s_cselect_b64 s[40:41], -1, 0
	s_add_i32 s2, 0, 0x20000
	v_or_b32_e32 v140, 16, v138
	v_or_b32_e32 v141, 32, v138
	v_or_b32_e32 v142, 48, v138
	v_add_u32_e32 v143, 0x80, v138
	v_add_u32_e32 v144, 0x90, v138
	v_add_u32_e32 v145, 0xa0, v138
	v_add_u32_e32 v146, 0xb0, v138
	v_or_b32_e32 v147, s29, v1
	v_add_u32_e32 v148, s2, v2
	s_mov_b32 s62, 0
	v_add_u32_e32 v149, 0, v3
	s_mov_b64 s[48:49], s[4:5]
	s_mov_b64 s[46:47], s[20:21]
	s_barrier
	s_waitcnt vmcnt(0)
	s_branch .LBB0_744

; template <class Desc, class Epi>
; __device__ __forceinline__ void gemm_phase(const int wv_, LAS unsigned char* lds, const Desc& d, const Epi& E) {
;     ...
; #pragma unroll
;         for (int a = 0; a < 2; ++a)
; #pragma unroll
;             for (int b = 0; b < 2; ++b)
; #pragma unroll
;                 for (int m = 0; m < 4; ++m)
; #pragma unroll
;                     for (int n = 0; n < 2; ++n) acc[a][b][m][n] = (f32x4){0.f, 0.f, 0.f, 0.f};
;         cur = nxt; cA = nA; cB = nB; ++ui;
;         if constexpr (Desc::GATHER) { voffA[0] = voffAn[0]; voffA[1] = voffAn[1]; voffA1[0] = voffAn1[0]; voffA1[1] = voffAn1[1]; }
.LBB0_746:
	s_add_u32 s2, s20, 0x80
	s_addc_u32 s3, s21, 0
	s_add_u32 s29, s4, 0x100
	v_mov_b32_e32 v12, 0
	s_addc_u32 s43, s5, 0
	s_mov_b32 s45, -2
	v_mov_b32_e32 v13, v12
	v_mov_b32_e32 v14, v12
	v_mov_b32_e32 v15, v12
	v_mov_b32_e32 v28, v12
	v_mov_b32_e32 v29, v12
	v_mov_b32_e32 v30, v12
	v_mov_b32_e32 v31, v12
	v_mov_b32_e32 v48, v12
	v_mov_b32_e32 v49, v12
	v_mov_b32_e32 v50, v12
	v_mov_b32_e32 v51, v12
	v_mov_b32_e32 v52, v12
	v_mov_b32_e32 v53, v12
	v_mov_b32_e32 v54, v12
	v_mov_b32_e32 v55, v12
	v_mov_b32_e32 v0, v12
	v_mov_b32_e32 v1, v12
	v_mov_b32_e32 v2, v12
	v_mov_b32_e32 v3, v12
	v_mov_b32_e32 v4, v12
	v_mov_b32_e32 v5, v12
	v_mov_b32_e32 v6, v12
	v_mov_b32_e32 v7, v12
	v_mov_b32_e32 v8, v12
	v_mov_b32_e32 v9, v12
	v_mov_b32_e32 v10, v12
	v_mov_b32_e32 v11, v12
	v_mov_b32_e32 v16, v12
	v_mov_b32_e32 v17, v12
	v_mov_b32_e32 v18, v12
	v_mov_b32_e32 v19, v12
	v_mov_b32_e32 v32, v12
	v_mov_b32_e32 v33, v12
	v_mov_b32_e32 v34, v12
	v_mov_b32_e32 v35, v12
	v_mov_b32_e32 v44, v12
	v_mov_b32_e32 v45, v12
	v_mov_b32_e32 v46, v12
	v_mov_b32_e32 v47, v12
	v_mov_b32_e32 v56, v12
	v_mov_b32_e32 v57, v12
	v_mov_b32_e32 v58, v12
	v_mov_b32_e32 v59, v12
	v_mov_b32_e32 v60, v12
	v_mov_b32_e32 v61, v12
	v_mov_b32_e32 v62, v12
	v_mov_b32_e32 v63, v12
	v_mov_b32_e32 v64, v12
	v_mov_b32_e32 v65, v12
	v_mov_b32_e32 v66, v12
	v_mov_b32_e32 v67, v12
	v_mov_b32_e32 v68, v12
	v_mov_b32_e32 v69, v12
	v_mov_b32_e32 v70, v12
	v_mov_b32_e32 v71, v12
	v_mov_b32_e32 v80, v12
	v_mov_b32_e32 v81, v12
	v_mov_b32_e32 v82, v12
	v_mov_b32_e32 v83, v12
	v_mov_b32_e32 v84, v12
	v_mov_b32_e32 v85, v12
	v_mov_b32_e32 v86, v12
	v_mov_b32_e32 v87, v12
	v_mov_b32_e32 v98, v12
	v_mov_b32_e32 v99, v12
	v_mov_b32_e32 v100, v12
	v_mov_b32_e32 v101, v12
	v_mov_b32_e32 v102, v12
	v_mov_b32_e32 v103, v12
	v_mov_b32_e32 v104, v12
	v_mov_b32_e32 v105, v12
	v_mov_b32_e32 v114, v12
	v_mov_b32_e32 v115, v12
	v_mov_b32_e32 v116, v12
	v_mov_b32_e32 v117, v12
	v_mov_b32_e32 v118, v12
	v_mov_b32_e32 v119, v12
	v_mov_b32_e32 v120, v12
	v_mov_b32_e32 v121, v12
	v_mov_b32_e32 v72, v12
	v_mov_b32_e32 v73, v12
	v_mov_b32_e32 v74, v12
	v_mov_b32_e32 v75, v12
	v_mov_b32_e32 v76, v12
	v_mov_b32_e32 v77, v12
	v_mov_b32_e32 v78, v12
	v_mov_b32_e32 v79, v12
	v_mov_b32_e32 v88, v12
	v_mov_b32_e32 v89, v12
	v_mov_b32_e32 v90, v12
	v_mov_b32_e32 v91, v12
	v_mov_b32_e32 v92, v12
	v_mov_b32_e32 v93, v12
	v_mov_b32_e32 v94, v12
	v_mov_b32_e32 v95, v12
	v_mov_b32_e32 v106, v12
	v_mov_b32_e32 v107, v12
	v_mov_b32_e32 v108, v12
	v_mov_b32_e32 v109, v12
	v_mov_b32_e32 v110, v12
	v_mov_b32_e32 v111, v12
	v_mov_b32_e32 v112, v12
	v_mov_b32_e32 v113, v12
	v_mov_b32_e32 v122, v12
	v_mov_b32_e32 v123, v12
	v_mov_b32_e32 v124, v12
	v_mov_b32_e32 v125, v12
	v_mov_b32_e32 v126, v12
	v_mov_b32_e32 v127, v12
	v_mov_b32_e32 v128, v12
	v_mov_b32_e32 v129, v12
	v_mov_b32_e32 v36, v12
	v_mov_b32_e32 v37, v12
	v_mov_b32_e32 v38, v12
	v_mov_b32_e32 v39, v12
	v_mov_b32_e32 v40, v12
	v_mov_b32_e32 v41, v12
	v_mov_b32_e32 v42, v12
	v_mov_b32_e32 v43, v12
	v_mov_b32_e32 v20, v12
	v_mov_b32_e32 v21, v12
	v_mov_b32_e32 v22, v12
	v_mov_b32_e32 v23, v12
	v_mov_b32_e32 v24, v12
	v_mov_b32_e32 v25, v12
	v_mov_b32_e32 v26, v12
	v_mov_b32_e32 v27, v12

; #define PG8_STAGE(bufoff, gbase, voff) do { _Pragma("unroll") for (int _i = 0; _i < 2; ++_i) \
;         __builtin_amdgcn_global_load_lds((const __attribute__((address_space(1))) unsigned*)((const __attribute__((address_space(1))) char*)(gbase) + (unsigned)lnd_v((int)(voff)[_i])), (LAS unsigned*)(lds + (bufoff) + ldsw + _i * 8192), 16, 0, 0); } while (0)
; #define PG8_WAIT_V(n) asm volatile("s_waitcnt vmcnt(" #n ")" ::: "memory")
; #define PG8_BAR __builtin_amdgcn_s_barrier()
; template <class Desc, class Epi>
; __device__ __forceinline__ void gemm_phase(const int wv_, LAS unsigned char* lds, const Desc& d, const Epi& E) {
;     ...
;     const unsigned ldsw = (unsigned)wid * 1024u;
;     const int aoff = lds_byte(wr * 64 + fr, fq * 8), boff = lds_byte(wc * 32 + fr, fq * 8);
;     ...
;     const char* cA = (const char*)cur.a; const char* cB = (const char*)cur.b;
;     PG8_STAGE(PG8_SB(0, 0), cB, voffB); PG8_STAGE(PG8_SB(0, 1), cB + hstepB, voffB); PG8_STAGE(PG8_SA(0, 0), cA, voffA); PG8_STAGE(PG8_SA(0, 1), cA, voffA1);
;     if (wr == 1) PG8_BAR;
;     PG8_WAIT_V(2); PG8_BAR;
;     PG8_STAGE(PG8_SB(1, 0), cB + kstep, voffB); PG8_STAGE(PG8_SA(1, 0), cA + kstep, voffA); PG8_STAGE(PG8_SB(1, 1), cB + hstepB + kstep, voffB);
;     PG8_WAIT_V(6); PG8_BAR;
.LBB0_884:
	s_and_b32 s1, 0xffff, s0
	s_and_b32 s0, 0xffff, s4
	s_add_u32 s40, s38, 0x49400000
	s_addc_u32 s41, s39, 0
	v_mov_b32_e32 v96, v205
	s_add_u32 s42, s38, 0x37a00000
	s_waitcnt vmcnt(2)
	s_barrier
	s_addc_u32 s43, s39, 0
	v_lshl_add_u64 v[0:1], s[56:57], 0, v[96:97]
	s_add_i32 m0, s69, 0x18000
	v_lshl_add_u64 v[0:1], v[0:1], 0, s[30:31]
	v_mov_b32_e32 v96, v208
	global_load_lds_dwordx4 v[0:1], off
	s_add_i32 m0, s69, 0x1a000
	v_lshl_add_u64 v[0:1], s[56:57], 0, v[96:97]
	v_lshl_add_u64 v[0:1], v[0:1], 0, s[30:31]
	v_mov_b32_e32 v96, v187
	global_load_lds_dwordx4 v[0:1], off
	s_add_i32 s74, s69, 0x8000
	v_lshl_add_u64 v[0:1], s[58:59], 0, v[96:97]
	s_lshl_b32 s3, s3, 5
	v_lshl_add_u64 v[0:1], v[0:1], 0, s[30:31]
	s_mov_b32 m0, s74
	v_mov_b32_e32 v96, v206
	s_and_b32 s73, s3, 0x60
	global_load_lds_dwordx4 v[0:1], off
	s_add_i32 s75, s69, 0xa000
	v_lshl_add_u64 v[0:1], s[58:59], 0, v[96:97]
	s_lshl_b32 s20, s2, 13
	s_lshl_b32 s3, s73, 7
	v_lshl_add_u64 v[0:1], v[0:1], 0, s[30:31]
	s_mov_b32 m0, s75
	s_add_u32 s4, s56, 0x10080
	global_load_lds_dwordx4 v[0:1], off
	v_mov_b32_e32 v0, v205
	s_addc_u32 s5, s57, 0
	s_add_i32 m0, s69, 0x1c000
	v_lshrrev_b32_e32 v1, 1, v4
	global_load_lds_dwordx4 v0, s[4:5]
	v_mov_b32_e32 v0, v208
	s_add_i32 m0, s69, 0x1e000
	v_and_b32_e32 v186, 24, v1
	global_load_lds_dwordx4 v0, s[4:5]
	v_and_b32_e32 v0, 15, v4
	v_lshlrev_b32_e32 v1, 1, v186
	v_lshl_or_b32 v209, s2, 6, v0
	v_lshl_or_b32 v0, v0, 6, v1
	v_lshlrev_b32_e32 v1, 2, v4
	v_and_b32_e32 v1, 32, v1
	s_waitcnt vmcnt(6)
	v_bitop3_b32 v2, v0, s20, v1 bitop3:0xde
	s_cmpk_lt_u32 s44, 0x100
	v_bitop3_b32 v210, v0, s3, v1 bitop3:0xde
	s_cselect_b64 s[44:45], -1, 0
	v_or_b32_e32 v211, 0xffffff80, v186
	v_or_b32_e32 v212, 16, v209
	v_or_b32_e32 v213, 32, v209
	v_or_b32_e32 v214, 48, v209
	v_add_u32_e32 v215, 0x80, v209
	v_add_u32_e32 v219, 0x90, v209
	v_add_u32_e32 v220, 0xa0, v209
	v_add_u32_e32 v221, 0xb0, v209
	s_mov_b32 s77, 0
	v_add_u32_e32 v222, 0, v2
	s_mov_b64 s[52:53], s[56:57]
	s_mov_b64 s[50:51], s[58:59]
	s_barrier
	s_waitcnt vmcnt(0)
	s_branch .LBB0_887

; template <class Desc, class Epi>
; __device__ __forceinline__ void gemm_phase(const int wv_, LAS unsigned char* lds, const Desc& d, const Epi& E) {
;     ...
; #pragma unroll
;         for (int a = 0; a < 2; ++a)
; #pragma unroll
;             for (int b = 0; b < 2; ++b)
; #pragma unroll
;                 for (int m = 0; m < 4; ++m)
; #pragma unroll
;                     for (int n = 0; n < 2; ++n) acc[a][b][m][n] = (f32x4){0.f, 0.f, 0.f, 0.f};
;         cur = nxt; cA = nA; cB = nB; ++ui;
;         if constexpr (Desc::GATHER) { voffA[0] = voffAn[0]; voffA[1] = voffAn[1]; voffA1[0] = voffAn1[0]; voffA1[1] = voffAn1[1]; }
.LBB0_889:
	v_mov_b32_e32 v8, 0
	s_mov_b32 s22, 0
	s_mov_b64 s[2:3], -1
	s_mov_b64 s[20:21], 0
	v_mov_b32_e32 v9, v8
	v_mov_b32_e32 v10, v8
	v_mov_b32_e32 v11, v8
	v_mov_b32_e32 v12, v8
	v_mov_b32_e32 v13, v8
	v_mov_b32_e32 v14, v8
	v_mov_b32_e32 v15, v8
	v_mov_b32_e32 v24, v8
	v_mov_b32_e32 v25, v8
	v_mov_b32_e32 v26, v8
	v_mov_b32_e32 v27, v8
	v_mov_b32_e32 v28, v8
	v_mov_b32_e32 v29, v8
	v_mov_b32_e32 v30, v8
	v_mov_b32_e32 v31, v8
	v_mov_b32_e32 v64, v8
	v_mov_b32_e32 v65, v8
	v_mov_b32_e32 v66, v8
	v_mov_b32_e32 v67, v8
	v_mov_b32_e32 v68, v8
	v_mov_b32_e32 v69, v8
	v_mov_b32_e32 v70, v8
	v_mov_b32_e32 v71, v8
	v_mov_b32_e32 v72, v8
	v_mov_b32_e32 v73, v8
	v_mov_b32_e32 v74, v8
	v_mov_b32_e32 v75, v8
	v_mov_b32_e32 v76, v8
	v_mov_b32_e32 v77, v8
	v_mov_b32_e32 v78, v8
	v_mov_b32_e32 v79, v8
	v_mov_b32_e32 v80, v8
	v_mov_b32_e32 v81, v8
	v_mov_b32_e32 v82, v8
	v_mov_b32_e32 v83, v8
	v_mov_b32_e32 v84, v8
	v_mov_b32_e32 v85, v8
	v_mov_b32_e32 v86, v8
	v_mov_b32_e32 v87, v8
	v_mov_b32_e32 v88, v8
	v_mov_b32_e32 v89, v8
	v_mov_b32_e32 v90, v8
	v_mov_b32_e32 v91, v8
	v_mov_b32_e32 v92, v8
	v_mov_b32_e32 v93, v8
	v_mov_b32_e32 v94, v8
	v_mov_b32_e32 v95, v8
	v_mov_b32_e32 v32, v8
	v_mov_b32_e32 v33, v8
	v_mov_b32_e32 v34, v8
	v_mov_b32_e32 v35, v8
	v_mov_b32_e32 v36, v8
	v_mov_b32_e32 v37, v8
	v_mov_b32_e32 v38, v8
	v_mov_b32_e32 v39, v8
	v_mov_b32_e32 v40, v8
	v_mov_b32_e32 v41, v8
	v_mov_b32_e32 v42, v8
	v_mov_b32_e32 v43, v8
	v_mov_b32_e32 v44, v8
	v_mov_b32_e32 v45, v8
	v_mov_b32_e32 v46, v8
	v_mov_b32_e32 v47, v8
	v_mov_b32_e32 v48, v8
	v_mov_b32_e32 v49, v8
	v_mov_b32_e32 v50, v8
	v_mov_b32_e32 v51, v8
	v_mov_b32_e32 v52, v8
	v_mov_b32_e32 v53, v8
	v_mov_b32_e32 v54, v8
	v_mov_b32_e32 v55, v8
	v_mov_b32_e32 v56, v8
	v_mov_b32_e32 v57, v8
	v_mov_b32_e32 v58, v8
	v_mov_b32_e32 v59, v8
	v_mov_b32_e32 v60, v8
	v_mov_b32_e32 v61, v8
	v_mov_b32_e32 v62, v8
	v_mov_b32_e32 v63, v8
	v_mov_b32_e32 v98, v8
	v_mov_b32_e32 v99, v8
	v_mov_b32_e32 v100, v8
	v_mov_b32_e32 v101, v8
	v_mov_b32_e32 v102, v8
	v_mov_b32_e32 v103, v8
	v_mov_b32_e32 v104, v8
	v_mov_b32_e32 v105, v8
	v_mov_b32_e32 v106, v8
	v_mov_b32_e32 v107, v8
	v_mov_b32_e32 v108, v8
	v_mov_b32_e32 v109, v8
	v_mov_b32_e32 v110, v8
	v_mov_b32_e32 v111, v8
	v_mov_b32_e32 v112, v8
	v_mov_b32_e32 v113, v8
	v_mov_b32_e32 v114, v8
	v_mov_b32_e32 v115, v8
	v_mov_b32_e32 v116, v8
	v_mov_b32_e32 v117, v8
	v_mov_b32_e32 v118, v8
	v_mov_b32_e32 v119, v8
	v_mov_b32_e32 v120, v8
	v_mov_b32_e32 v121, v8
	v_mov_b32_e32 v122, v8
	v_mov_b32_e32 v123, v8
	v_mov_b32_e32 v124, v8
	v_mov_b32_e32 v125, v8
	v_mov_b32_e32 v126, v8
	v_mov_b32_e32 v127, v8
	v_mov_b32_e32 v128, v8
	v_mov_b32_e32 v129, v8
	v_mov_b32_e32 v20, v8
	v_mov_b32_e32 v21, v8
	v_mov_b32_e32 v22, v8
	v_mov_b32_e32 v23, v8
	v_mov_b32_e32 v16, v8
	v_mov_b32_e32 v17, v8
	v_mov_b32_e32 v18, v8
	v_mov_b32_e32 v19, v8
	v_mov_b32_e32 v4, v8
	v_mov_b32_e32 v5, v8
	v_mov_b32_e32 v6, v8
	v_mov_b32_e32 v7, v8
	v_mov_b32_e32 v0, v8
	v_mov_b32_e32 v1, v8
	v_mov_b32_e32 v2, v8
	v_mov_b32_e32 v3, v8

; #define PG8_STAGE(bufoff, gbase, voff) do { _Pragma("unroll") for (int _i = 0; _i < 2; ++_i) \
;         __builtin_amdgcn_global_load_lds((const __attribute__((address_space(1))) unsigned*)((const __attribute__((address_space(1))) char*)(gbase) + (unsigned)lnd_v((int)(voff)[_i])), (LAS unsigned*)(lds + (bufoff) + ldsw + _i * 8192), 16, 0, 0); } while (0)
; #define PG8_WAIT_V(n) asm volatile("s_waitcnt vmcnt(" #n ")" ::: "memory")
; #define PG8_BAR __builtin_amdgcn_s_barrier()
; template <class Desc, class Epi>
; __device__ __forceinline__ void gemm_phase(const int wv_, LAS unsigned char* lds, const Desc& d, const Epi& E) {
;     ...
;     const unsigned ldsw = (unsigned)wid * 1024u;
;     const int aoff = lds_byte(wr * 64 + fr, fq * 8), boff = lds_byte(wc * 32 + fr, fq * 8);
;     ...
;     const char* cA = (const char*)cur.a; const char* cB = (const char*)cur.b;
;     PG8_STAGE(PG8_SB(0, 0), cB, voffB); PG8_STAGE(PG8_SB(0, 1), cB + hstepB, voffB); PG8_STAGE(PG8_SA(0, 0), cA, voffA); PG8_STAGE(PG8_SA(0, 1), cA, voffA1);
;     if (wr == 1) PG8_BAR;
;     PG8_WAIT_V(2); PG8_BAR;
;     PG8_STAGE(PG8_SB(1, 0), cB + kstep, voffB); PG8_STAGE(PG8_SA(1, 0), cA + kstep, voffA); PG8_STAGE(PG8_SB(1, 1), cB + hstepB + kstep, voffB);
;     PG8_WAIT_V(6); PG8_BAR;
.LBB0_911:
	v_readlane_b32 s22, v254, 57
	s_lshl_b32 s21, s22, 5
	s_lshl_b32 s20, s20, 2
	s_or_b32 s20, s20, s21
	s_or_b32 s1, s20, s1
	v_mov_b32_e32 v96, v134
	s_add_u32 s40, s38, 0x3b200000
	s_waitcnt vmcnt(2)
	s_barrier
	s_addc_u32 s41, s39, 0
	v_lshl_add_u64 v[2:3], s[50:51], 0, v[96:97]
	s_add_i32 m0, s61, 0x18000
	v_lshl_add_u64 v[2:3], v[2:3], 0, s[30:31]
	v_mov_b32_e32 v96, v137
	global_load_lds_dwordx4 v[2:3], off
	s_add_i32 m0, s61, 0x1a000
	v_lshl_add_u64 v[2:3], s[50:51], 0, v[96:97]
	v_lshl_add_u64 v[2:3], v[2:3], 0, s[30:31]
	v_mov_b32_e32 v96, v132
	s_lshl_b32 s3, s3, 5
	global_load_lds_dwordx4 v[2:3], off
	s_add_i32 s68, s61, 0x8000
	v_lshl_add_u64 v[2:3], s[52:53], 0, v[96:97]
	s_mov_b32 s24, s22
	s_and_b32 s3, s3, 0x60
	v_lshl_add_u64 v[2:3], v[2:3], 0, s[30:31]
	s_mov_b32 m0, s68
	v_mov_b32_e32 v96, v135
	s_add_i32 s66, s5, 0xffffff80
	s_lshl_b32 s5, s2, 13
	s_lshl_b32 s22, s3, 7
	s_lshl_b32 s67, s24, 7
	global_load_lds_dwordx4 v[2:3], off
	s_add_i32 s69, s61, 0xa000
	v_lshl_add_u64 v[2:3], s[52:53], 0, v[96:97]
	v_lshl_add_u64 v[2:3], v[2:3], 0, s[30:31]
	s_mov_b32 m0, s69
	s_add_u32 s20, s50, 0x40080
	v_mov_b32_e32 v1, v134
	global_load_lds_dwordx4 v[2:3], off
	s_addc_u32 s21, s51, 0
	s_add_i32 m0, s61, 0x1c000
	v_lshrrev_b32_e32 v2, 1, v0
	global_load_lds_dwordx4 v1, s[20:21]
	v_mov_b32_e32 v1, v137
	s_add_i32 m0, s61, 0x1e000
	v_and_b32_e32 v2, 24, v2
	global_load_lds_dwordx4 v1, s[20:21]
	v_and_b32_e32 v1, 15, v0
	v_lshl_or_b32 v138, s2, 6, v1
	v_lshlrev_b32_e32 v3, 1, v2
	v_lshl_or_b32 v1, v1, 6, v3
	v_lshlrev_b32_e32 v3, 2, v138
	v_and_b32_e32 v4, 32, v3
	v_lshlrev_b32_e32 v0, 2, v0
	s_waitcnt vmcnt(6)
	s_cmpk_lt_u32 s4, 0x100
	v_bitop3_b32 v4, v1, s5, v4 bitop3:0xde
	v_and_b32_e32 v0, 32, v0
	s_cselect_b64 s[42:43], -1, 0
	s_add_i32 s2, 0, 0x20000
	v_bitop3_b32 v139, v1, s22, v0 bitop3:0xde
	v_or_b32_e32 v140, 16, v138
	v_or_b32_e32 v141, 32, v138
	v_or_b32_e32 v142, 48, v138
	v_add_u32_e32 v143, 0x80, v138
	v_add_u32_e32 v144, 0x90, v138
	v_add_u32_e32 v145, 0xa0, v138
	v_add_u32_e32 v146, 0xb0, v138
	v_or_b32_e32 v147, s3, v2
	v_add_u32_e32 v148, s2, v3
	s_mov_b32 s73, 0
	v_add_u32_e32 v149, 0, v4
	s_mov_b64 s[46:47], s[50:51]
	s_mov_b64 s[44:45], s[52:53]
	v_readlane_b32 s23, v254, 58
	s_barrier
	s_waitcnt vmcnt(0)
	s_branch .LBB0_914

; template <class Desc, class Epi>
; __device__ __forceinline__ void gemm_phase(const int wv_, LAS unsigned char* lds, const Desc& d, const Epi& E) {
;     ...
; #pragma unroll
;         for (int a = 0; a < 2; ++a)
; #pragma unroll
;             for (int b = 0; b < 2; ++b)
; #pragma unroll
;                 for (int m = 0; m < 4; ++m)
; #pragma unroll
;                     for (int n = 0; n < 2; ++n) acc[a][b][m][n] = (f32x4){0.f, 0.f, 0.f, 0.f};
;         cur = nxt; cA = nA; cB = nB; ++ui;
;         if constexpr (Desc::GATHER) { voffA[0] = voffAn[0]; voffA[1] = voffAn[1]; voffA1[0] = voffAn1[0]; voffA1[1] = voffAn1[1]; }
.LBB0_916:
	v_mov_b32_e32 v12, 0
	s_mov_b32 s22, 0
	s_mov_b64 s[2:3], -1
	s_mov_b64 s[20:21], 0
	v_mov_b32_e32 v13, v12
	v_mov_b32_e32 v14, v12
	v_mov_b32_e32 v15, v12
	v_mov_b32_e32 v28, v12
	v_mov_b32_e32 v29, v12
	v_mov_b32_e32 v30, v12
	v_mov_b32_e32 v31, v12
	v_mov_b32_e32 v48, v12
	v_mov_b32_e32 v49, v12
	v_mov_b32_e32 v50, v12
	v_mov_b32_e32 v51, v12
	v_mov_b32_e32 v52, v12
	v_mov_b32_e32 v53, v12
	v_mov_b32_e32 v54, v12
	v_mov_b32_e32 v55, v12
	v_mov_b32_e32 v0, v12
	v_mov_b32_e32 v1, v12
	v_mov_b32_e32 v2, v12
	v_mov_b32_e32 v3, v12
	v_mov_b32_e32 v4, v12
	v_mov_b32_e32 v5, v12
	v_mov_b32_e32 v6, v12
	v_mov_b32_e32 v7, v12
	v_mov_b32_e32 v8, v12
	v_mov_b32_e32 v9, v12
	v_mov_b32_e32 v10, v12
	v_mov_b32_e32 v11, v12
	v_mov_b32_e32 v16, v12
	v_mov_b32_e32 v17, v12
	v_mov_b32_e32 v18, v12
	v_mov_b32_e32 v19, v12
	v_mov_b32_e32 v32, v12
	v_mov_b32_e32 v33, v12
	v_mov_b32_e32 v34, v12
	v_mov_b32_e32 v35, v12
	v_mov_b32_e32 v44, v12
	v_mov_b32_e32 v45, v12
	v_mov_b32_e32 v46, v12
	v_mov_b32_e32 v47, v12
	v_mov_b32_e32 v56, v12
	v_mov_b32_e32 v57, v12
	v_mov_b32_e32 v58, v12
	v_mov_b32_e32 v59, v12
	v_mov_b32_e32 v60, v12
	v_mov_b32_e32 v61, v12
	v_mov_b32_e32 v62, v12
	v_mov_b32_e32 v63, v12
	v_mov_b32_e32 v64, v12
	v_mov_b32_e32 v65, v12
	v_mov_b32_e32 v66, v12
	v_mov_b32_e32 v67, v12
	v_mov_b32_e32 v68, v12
	v_mov_b32_e32 v69, v12
	v_mov_b32_e32 v70, v12
	v_mov_b32_e32 v71, v12
	v_mov_b32_e32 v80, v12
	v_mov_b32_e32 v81, v12
	v_mov_b32_e32 v82, v12
	v_mov_b32_e32 v83, v12
	v_mov_b32_e32 v84, v12
	v_mov_b32_e32 v85, v12
	v_mov_b32_e32 v86, v12
	v_mov_b32_e32 v87, v12
	v_mov_b32_e32 v98, v12
	v_mov_b32_e32 v99, v12
	v_mov_b32_e32 v100, v12
	v_mov_b32_e32 v101, v12
	v_mov_b32_e32 v102, v12
	v_mov_b32_e32 v103, v12
	v_mov_b32_e32 v104, v12
	v_mov_b32_e32 v105, v12
	v_mov_b32_e32 v114, v12
	v_mov_b32_e32 v115, v12
	v_mov_b32_e32 v116, v12
	v_mov_b32_e32 v117, v12
	v_mov_b32_e32 v118, v12
	v_mov_b32_e32 v119, v12
	v_mov_b32_e32 v120, v12
	v_mov_b32_e32 v121, v12
	v_mov_b32_e32 v72, v12
	v_mov_b32_e32 v73, v12
	v_mov_b32_e32 v74, v12
	v_mov_b32_e32 v75, v12
	v_mov_b32_e32 v76, v12
	v_mov_b32_e32 v77, v12
	v_mov_b32_e32 v78, v12
	v_mov_b32_e32 v79, v12
	v_mov_b32_e32 v88, v12
	v_mov_b32_e32 v89, v12
	v_mov_b32_e32 v90, v12
	v_mov_b32_e32 v91, v12
	v_mov_b32_e32 v92, v12
	v_mov_b32_e32 v93, v12
	v_mov_b32_e32 v94, v12
	v_mov_b32_e32 v95, v12
	v_mov_b32_e32 v106, v12
	v_mov_b32_e32 v107, v12
	v_mov_b32_e32 v108, v12
	v_mov_b32_e32 v109, v12
	v_mov_b32_e32 v110, v12
	v_mov_b32_e32 v111, v12
	v_mov_b32_e32 v112, v12
	v_mov_b32_e32 v113, v12
	v_mov_b32_e32 v122, v12
	v_mov_b32_e32 v123, v12
	v_mov_b32_e32 v124, v12
	v_mov_b32_e32 v125, v12
	v_mov_b32_e32 v126, v12
	v_mov_b32_e32 v127, v12
	v_mov_b32_e32 v128, v12
	v_mov_b32_e32 v129, v12
	v_mov_b32_e32 v36, v12
	v_mov_b32_e32 v37, v12
	v_mov_b32_e32 v38, v12
	v_mov_b32_e32 v39, v12
	v_mov_b32_e32 v40, v12
	v_mov_b32_e32 v41, v12
	v_mov_b32_e32 v42, v12
	v_mov_b32_e32 v43, v12
	v_mov_b32_e32 v20, v12
	v_mov_b32_e32 v21, v12
	v_mov_b32_e32 v22, v12
	v_mov_b32_e32 v23, v12
	v_mov_b32_e32 v24, v12
	v_mov_b32_e32 v25, v12
	v_mov_b32_e32 v26, v12
	v_mov_b32_e32 v27, v12

; #define PG8_STAGE(bufoff, gbase, voff) do { _Pragma("unroll") for (int _i = 0; _i < 2; ++_i) \
;         __builtin_amdgcn_global_load_lds((const __attribute__((address_space(1))) unsigned*)((const __attribute__((address_space(1))) char*)(gbase) + (unsigned)lnd_v((int)(voff)[_i])), (LAS unsigned*)(lds + (bufoff) + ldsw + _i * 8192), 16, 0, 0); } while (0)
; #define PG8_WAIT_V(n) asm volatile("s_waitcnt vmcnt(" #n ")" ::: "memory")
; #define PG8_BAR __builtin_amdgcn_s_barrier()
; template <class Desc, class Epi>
; __device__ __forceinline__ void gemm_phase(const int wv_, LAS unsigned char* lds, const Desc& d, const Epi& E) {
;     ...
;     const unsigned ldsw = (unsigned)wid * 1024u;
;     const int aoff = lds_byte(wr * 64 + fr, fq * 8), boff = lds_byte(wc * 32 + fr, fq * 8);
;     ...
;     const char* cA = (const char*)cur.a; const char* cB = (const char*)cur.b;
;     PG8_STAGE(PG8_SB(0, 0), cB, voffB); PG8_STAGE(PG8_SB(0, 1), cB + hstepB, voffB); PG8_STAGE(PG8_SA(0, 0), cA, voffA); PG8_STAGE(PG8_SA(0, 1), cA, voffA1);
;     if (wr == 1) PG8_BAR;
;     PG8_WAIT_V(2); PG8_BAR;
;     PG8_STAGE(PG8_SB(1, 0), cB + kstep, voffB); PG8_STAGE(PG8_SA(1, 0), cA + kstep, voffA); PG8_STAGE(PG8_SB(1, 1), cB + hstepB + kstep, voffB);
;     PG8_WAIT_V(6); PG8_BAR;
.LBB0_931:
	s_lshl_b32 s1, s1, 2
	s_or_b32 s1, s1, s5
	v_mov_b32_e32 v96, v134
	s_add_u32 s38, s38, 0x3f200000
	s_waitcnt vmcnt(2)
	s_barrier
	s_addc_u32 s39, s39, 0
	v_lshl_add_u64 v[2:3], s[48:49], 0, v[96:97]
	s_add_i32 m0, s60, 0x18000
	v_lshl_add_u64 v[2:3], v[2:3], 0, s[30:31]
	v_mov_b32_e32 v96, v137
	global_load_lds_dwordx4 v[2:3], off
	s_add_i32 m0, s60, 0x1a000
	v_lshl_add_u64 v[2:3], s[48:49], 0, v[96:97]
	v_lshl_add_u64 v[2:3], v[2:3], 0, s[30:31]
	v_mov_b32_e32 v96, v132
	s_lshl_b32 s3, s3, 5
	global_load_lds_dwordx4 v[2:3], off
	s_add_i32 s65, s60, 0x8000
	v_lshl_add_u64 v[2:3], s[50:51], 0, v[96:97]
	s_and_b32 s3, s3, 0x60
	v_lshl_add_u64 v[2:3], v[2:3], 0, s[30:31]
	s_mov_b32 m0, s65
	v_mov_b32_e32 v96, v135
	s_lshl_b32 s5, s2, 13
	s_lshl_b32 s22, s3, 7
	global_load_lds_dwordx4 v[2:3], off
	s_add_i32 s66, s60, 0xa000
	v_lshl_add_u64 v[2:3], s[50:51], 0, v[96:97]
	v_lshl_add_u64 v[2:3], v[2:3], 0, s[30:31]
	s_mov_b32 m0, s66
	s_add_u32 s20, s48, 0x40080
	v_mov_b32_e32 v1, v134
	global_load_lds_dwordx4 v[2:3], off
	s_addc_u32 s21, s49, 0
	s_add_i32 m0, s60, 0x1c000
	v_lshrrev_b32_e32 v2, 1, v0
	global_load_lds_dwordx4 v1, s[20:21]
	v_mov_b32_e32 v1, v137
	s_add_i32 m0, s60, 0x1e000
	v_and_b32_e32 v2, 24, v2
	global_load_lds_dwordx4 v1, s[20:21]
	v_and_b32_e32 v1, 15, v0
	v_lshl_or_b32 v138, s2, 6, v1
	v_lshlrev_b32_e32 v3, 1, v2
	v_lshl_or_b32 v1, v1, 6, v3
	v_lshlrev_b32_e32 v3, 2, v138
	v_and_b32_e32 v4, 32, v3
	v_lshlrev_b32_e32 v0, 2, v0
	s_waitcnt vmcnt(6)
	s_cmpk_lt_u32 s4, 0x100
	v_bitop3_b32 v4, v1, s5, v4 bitop3:0xde
	v_and_b32_e32 v0, 32, v0
	s_cselect_b64 s[40:41], -1, 0
	s_add_i32 s2, 0, 0x20000
	v_bitop3_b32 v139, v1, s22, v0 bitop3:0xde
	v_or_b32_e32 v140, 16, v138
	v_or_b32_e32 v141, 32, v138
	v_or_b32_e32 v142, 48, v138
	v_add_u32_e32 v143, 0x80, v138
	v_add_u32_e32 v144, 0x90, v138
	v_add_u32_e32 v145, 0xa0, v138
	v_add_u32_e32 v146, 0xb0, v138
	v_or_b32_e32 v147, s3, v2
	v_add_u32_e32 v148, s2, v3
	s_mov_b32 s70, 0
	v_add_u32_e32 v149, 0, v4
	s_mov_b64 s[44:45], s[48:49]
	s_mov_b64 s[42:43], s[50:51]
	s_barrier
	s_waitcnt vmcnt(0)
	s_branch .LBB0_934

; #define TID() (lnd_s(wv_) * 64 + (int)__builtin_amdgcn_mbcnt_hi(~0u, __builtin_amdgcn_mbcnt_lo(~0u, (unsigned)lnd_s(0))))
; __device__ __forceinline__ int v_rd_base(int lane) { const int g = lane >> 4, c = lane & 15; return (8 * (g >> 1) + (c >> 2)) * KPITCH + (16 * (g & 1) + 4 * (c & 3)) * 2; }
; #define SLOAD(k0) do { \
;     ks0 = *(const bf16x8*)(&Kh[(long)(k0) * LDK + kg[0]]); ks1 = *(const bf16x8*)(&Kh[(long)(k0) * LDK + kg[1]]); ks2 = *(const bf16x8*)(&Kh[(long)(k0) * LDK + kg[2]]); } while (0)
; #define SWRITE(b) do { \
;     *(bf16x8*)(K_lds + (b) * SHM_K + kl[0]) = ks0; *(bf16x8*)(K_lds + (b) * SHM_K + kl[1]) = ks1; *(bf16x8*)(K_lds + (b) * SHM_K + kl[2]) = ks2; } while (0)
; #define SWAIT() asm volatile("s_waitcnt vmcnt(0)" ::: "memory")
; template <int VAR> __device__ __forceinline__ void attn_dense_body(const int wv_, const bf16_t* __restrict__ Qb, const bf16_t* __restrict__ Kh, const bf16_t* __restrict__ Vh, bf16_t* __restrict__ Ob, int seq, unsigned char* lds) {
;     const int tid = TID(), wid = tid >> 6, lane = tid & 63, r32 = lane & 31, hi = lane >> 5;
;     unsigned char* K_lds = lds;
;     float* ws = (float*)(lds + 2 * SHM_K) + wid * 64; float* li_l = ws; float* al_l = ws + 32;
;     float m_reg = -1e30f, l_reg = 0; f32x16 o[4] = {}; bf16x8 qr[12];
;     const bf16_t* Qw = Qb + (long)(wid * QBLK + r32) * LDQ + hi * 8;
; #pragma unroll
;     for (int d0 = 0; d0 < 12; ++d0) qr[d0] = *(const bf16x8*)(Qw + d0 * 16);
;     int kg[3], kl[3];
; #pragma unroll
;     for (int i = 0; i < 3; ++i) { const int id = tid + 512 * i, row = id / 24, ch = id % 24; kg[i] = row * LDK + ch * 8; kl[i] = KSWZ(row, ch * 16); }
;     const int vb0 = (int)(uintptr_t)K_lds + v_rd_base(lane);
;     bf16x8 ks0, ks1, ks2;
;     ...
;     f32x16 p0, p1; float mn, al; bf16x8 pa0, pa1, pa2, pa3; const int NT = seq / KVBLK;
;     SLOAD(0); SWAIT(); SWRITE(0); SLOAD(KVBLK);
.LBB0_998:
	v_readlane_b32 s36, v254, 5
	s_mov_b32 s37, 0
	s_lshl_b32 s0, s5, 5
	v_mbcnt_lo_u32_b32 v0, -1, s37
	v_mbcnt_hi_u32_b32 v166, -1, v0
	v_lshl_add_u32 v26, s36, 6, v166
	s_mov_b32 s37, 0x2aaaaaab
	v_mul_hi_i32 v0, v26, s37
	v_lshrrev_b32_e32 v1, 31, v0
	v_ashrrev_i32_e32 v0, 2, v0
	s_and_b32 s0, s0, 0xe0
	s_and_b32 s1, s5, 0xffffff00
	v_add_u32_e32 v27, v0, v1
	v_add_u32_e32 v1, 0x200, v26
	s_or_b32 s0, s0, s1
	s_bfe_u32 s1, s5, 0x50003
	v_mul_hi_i32 v2, v1, s37
	s_or_b32 s2, s0, s1
	v_lshrrev_b32_e32 v3, 31, v2
	v_ashrrev_i32_e32 v2, 2, v2
	s_and_b64 s[0:1], s[42:43], exec
	v_add_u32_e32 v29, v2, v3
	s_cselect_b32 s2, s2, s5
	s_movk_i32 s36, 0xc0
	v_mul_lo_u32 v2, v29, 24
	s_ashr_i32 s44, s2, 4
	v_sub_u32_e32 v30, v1, v2
	v_mul_lo_u32 v1, v29, s36
	s_ashr_i32 s46, s2, 6
	s_ashr_i32 s45, s44, 31
	s_lshl_b32 s2, s2, 8
	v_lshl_add_u32 v2, v30, 3, v1
	v_add_u32_e32 v1, 0x400, v26
	s_lshl_b64 s[0:1], s[44:45], 12
	s_and_b32 s45, s2, 0xf00
	v_mul_hi_i32 v3, v1, s37
	s_or_b32 s0, s0, s45
	v_lshrrev_b32_e32 v4, 31, v3
	v_ashrrev_i32_e32 v3, 2, v3
	s_mulk_i32 s1, 0x180
	s_mul_hi_u32 s2, s0, 0x180
	v_add_u32_e32 v31, v3, v4
	s_add_i32 s1, s2, s1
	s_mulk_i32 s0, 0x180
	v_mul_lo_u32 v0, v27, 24
	v_mul_lo_u32 v3, v31, 24
	s_add_u32 s2, s21, s0
	v_sub_u32_e32 v28, v26, v0
	v_mul_lo_u32 v0, v27, s36
	v_sub_u32_e32 v32, v1, v3
	v_mul_lo_u32 v1, v31, s36
	s_addc_u32 s3, s22, s1
	s_ashr_i32 s47, s46, 31
	s_mul_i32 s38, s46, 0x180000
	v_ashrrev_i32_e32 v170, 6, v26
	v_lshl_add_u32 v0, v28, 3, v0
	v_lshl_add_u32 v8, v32, 3, v1
	s_mul_hi_i32 s29, s46, 0x180000
	s_add_u32 s0, s23, s38
	v_and_b32_e32 v168, 31, v166
	v_lshlrev_b32_e32 v158, 5, v170
	v_ashrrev_i32_e32 v1, 31, v0
	v_ashrrev_i32_e32 v3, 31, v2
	v_ashrrev_i32_e32 v9, 31, v8
	s_addc_u32 s1, s24, s29
	v_bfe_u32 v169, v166, 5, 1
	v_lshlrev_b64 v[12:13], 1, v[0:1]
	v_lshlrev_b64 v[16:17], 1, v[2:3]
	v_lshlrev_b64 v[20:21], 1, v[8:9]
	v_or_b32_e32 v33, v158, v168
	v_mov_b64_e32 v[24:25], s[2:3]
	v_lshl_add_u64 v[14:15], s[0:1], 0, v[12:13]
	v_lshl_add_u64 v[18:19], s[0:1], 0, v[16:17]
	v_lshl_add_u64 v[22:23], s[0:1], 0, v[20:21]
	v_mad_i64_i32 v[24:25], s[0:1], v33, s28, v[24:25]
	v_lshlrev_b32_e32 v96, 4, v169
	v_lshl_add_u64 v[24:25], v[24:25], 0, v[96:97]
	global_load_dwordx4 v[0:3], v[14:15], off
	global_load_dwordx4 v[4:7], v[18:19], off
	global_load_dwordx4 v[8:11], v[22:23], off
	global_load_dwordx4 v[142:145], v[24:25], off
	global_load_dwordx4 v[138:141], v[24:25], off offset:32
	global_load_dwordx4 v[134:137], v[24:25], off offset:64
	global_load_dwordx4 v[130:133], v[24:25], off offset:96
	global_load_dwordx4 v[126:129], v[24:25], off offset:128
	global_load_dwordx4 v[122:125], v[24:25], off offset:160
	global_load_dwordx4 v[118:121], v[24:25], off offset:192
	global_load_dwordx4 v[114:117], v[24:25], off offset:224
	global_load_dwordx4 v[110:113], v[24:25], off offset:256
	global_load_dwordx4 v[106:109], v[24:25], off offset:288
	global_load_dwordx4 v[102:105], v[24:25], off offset:320
	global_load_dwordx4 v[98:101], v[24:25], off offset:352
	s_movk_i32 s0, 0x6000
	v_add_co_u32_e32 v14, vcc, s0, v14
	s_waitcnt vmcnt(0)
	s_movk_i32 s1, 0x190
	s_nop 0
	v_addc_co_u32_e32 v15, vcc, 0, v15, vcc
	v_add_co_u32_e32 v18, vcc, s0, v18
	s_cmp_lg_u32 0, -1
	s_nop 0
	v_addc_co_u32_e32 v19, vcc, 0, v19, vcc
	global_load_dwordx4 v[146:149], v[14:15], off
	global_load_dwordx4 v[150:153], v[18:19], off
	v_add_co_u32_e32 v14, vcc, s0, v22
	v_lshlrev_b32_e32 v18, 2, v166
	s_nop 0
	v_addc_co_u32_e32 v15, vcc, 0, v23, vcc
	global_load_dwordx4 v[154:157], v[14:15], off
	v_and_b32_e32 v14, 0x3fffffc0, v26
	v_lshl_add_u32 v159, v14, 2, 0
	v_mul_lo_u32 v14, v27, s1
	v_lshl_add_u32 v175, v28, 4, v14
	v_mul_lo_u32 v14, v29, s1
	v_lshl_add_u32 v176, v30, 4, v14
	v_mul_lo_u32 v14, v31, s1
	v_lshl_add_u32 v177, v32, 4, v14
	v_lshrrev_b32_e32 v14, 2, v166
	v_and_b32_e32 v15, 16, v166
	v_and_b32_e32 v14, 11, v14
	v_and_or_b32 v15, v18, 12, v15
	v_add_u32_e32 v18, 0, v175
	v_mul_u32_u24_e32 v14, 0x190, v14
	v_lshlrev_b32_e32 v15, 1, v15
	v_mad_u32_u24 v178, v168, s1, v96
	s_cselect_b32 s1, 0, 0
	s_add_u32 s2, s25, s38
	v_add3_u32 v172, v14, s1, v15
	s_addc_u32 s3, s48, s29
	v_mov_b32_e32 v14, v97
	v_mov_b32_e32 v15, v97
	v_and_b32_e32 v167, 63, v166
	v_lshl_add_u64 v[160:161], s[2:3], 0, v[20:21]
	v_lshl_add_u64 v[162:163], s[2:3], 0, v[16:17]
	v_lshl_add_u64 v[164:165], s[2:3], 0, v[12:13]
	v_mov_b32_e32 v12, v97
	v_mov_b32_e32 v13, v97
	s_mov_b32 s0, 0
	v_cmp_gt_u32_e64 s[36:37], 32, v167
	v_lshl_add_u32 v171, v168, 2, v159
	v_mov_b32_e32 v179, 0
	v_mov_b32_e32 v173, 0xf149f2ca
	s_mov_b64 s[2:3], 0
	s_waitcnt vmcnt(3)
	ds_write_b128 v18, v[0:3]
	v_add_u32_e32 v0, 0, v176
	ds_write_b128 v0, v[4:7]
	v_add_u32_e32 v0, 0, v177
	ds_write_b128 v0, v[8:11]
	v_mov_b32_e32 v0, v97
	v_mov_b32_e32 v1, v97
	v_mov_b32_e32 v2, v97
	v_mov_b32_e32 v3, v97
	v_mov_b32_e32 v4, v97
	v_mov_b32_e32 v5, v97
	v_mov_b32_e32 v6, v97
	v_mov_b32_e32 v7, v97
	v_mov_b32_e32 v8, v97
	v_mov_b32_e32 v9, v97
	v_mov_b32_e32 v10, v97
	v_mov_b32_e32 v11, v97
	v_mov_b64_e32 v[62:63], v[14:15]
	v_mov_b64_e32 v[46:47], v[14:15]
	v_mov_b64_e32 v[30:31], v[14:15]
	v_mov_b64_e32 v[60:61], v[12:13]
	v_mov_b64_e32 v[58:59], v[10:11]
	v_mov_b64_e32 v[56:57], v[8:9]
	v_mov_b64_e32 v[54:55], v[6:7]
	v_mov_b64_e32 v[52:53], v[4:5]
	v_mov_b64_e32 v[50:51], v[2:3]
	v_mov_b64_e32 v[48:49], v[0:1]
	v_mov_b64_e32 v[44:45], v[12:13]
	v_mov_b64_e32 v[42:43], v[10:11]
	v_mov_b64_e32 v[40:41], v[8:9]
	v_mov_b64_e32 v[38:39], v[6:7]
	v_mov_b64_e32 v[36:37], v[4:5]
	v_mov_b64_e32 v[34:35], v[2:3]
	v_mov_b64_e32 v[32:33], v[0:1]
	v_mov_b64_e32 v[28:29], v[12:13]
	v_mov_b64_e32 v[26:27], v[10:11]
	v_mov_b64_e32 v[24:25], v[8:9]
	v_mov_b64_e32 v[22:23], v[6:7]
	v_mov_b64_e32 v[20:21], v[4:5]
	v_mov_b64_e32 v[18:19], v[2:3]
	v_mov_b64_e32 v[16:17], v[0:1]

; __device__ __forceinline__ void partialSM(f32x16& p0, f32x16& p1, float& m_reg, float& mn, float& alpha) {
;     constexpr float C = SCALE * 1.4426950408889634f;
;     float pmax = p0[0];
; #pragma unroll
;     for (int r = 1; r < 16; ++r) pmax = fmaxf(pmax, p0[r]);
; #pragma unroll
;     for (int r = 0; r < 16; ++r) pmax = fmaxf(pmax, p1[r]);
;     { auto rr = __builtin_amdgcn_permlane32_swap(__float_as_uint(pmax), __float_as_uint(pmax), false, false);
;       pmax = fmaxf(__uint_as_float(rr[0]), __uint_as_float(rr[1])); }
;     if (__builtin_expect(__all(pmax - m_reg <= THR / SCALE), 1)) { mn = m_reg; alpha = 1.f; }
;     else { mn = fmaxf(m_reg, pmax); alpha = __builtin_amdgcn_exp2f((m_reg - mn) * C); m_reg = mn; }
;     const float mnC = -mn * C;
; #pragma unroll
;     for (int r = 0; r < 16; ++r) p0[r] = fmaf(p0[r], C, mnC);
; #pragma unroll
;     for (int r = 0; r < 16; ++r) p1[r] = fmaf(p1[r], C, mnC);
; #pragma unroll
;     for (int r = 0; r < 16; ++r) p0[r] = __builtin_amdgcn_exp2f(p0[r]);
; }
; __device__ __forceinline__ void finishSM(f32x16& p0, f32x16& p1, float alpha, float& l_reg, bf16x8& pa0, bf16x8& pa1, bf16x8& pa2, bf16x8& pa3) {
; #pragma unroll
;     for (int r = 0; r < 16; ++r) p1[r] = __builtin_amdgcn_exp2f(p1[r]);
;     float ps = 0;
; #pragma unroll
;     for (int r = 0; r < 16; ++r) ps += p0[r];
; #pragma unroll
;     for (int r = 0; r < 16; ++r) ps += p1[r];
;     { auto rr = __builtin_amdgcn_permlane32_swap(__float_as_uint(ps), __float_as_uint(ps), false, false);
;       ps = __uint_as_float(rr[0]) + __uint_as_float(rr[1]); }
;     l_reg = l_reg * alpha + ps;
;     ...
;     PK4(p0, 0, pa0); PK4(p0, 8, pa1); PK4(p1, 0, pa2); PK4(p1, 8, pa3);
;     ...
; }
; template <int OFF> __device__ __forceinline__ bf16x8 k_read(int kb) { bf16x8 r; asm volatile("ds_read_b128 %0, %1 offset:%2" : "=&v"(r) : "v"(kb), "i"(OFF) : "memory"); return r; }
; __device__ __forceinline__ void qkt(f32x16& p0, f32x16& p1, const unsigned char* Ks, const bf16x8* qr, int r32, int hi) {
;     const int kb = (int)(uintptr_t)Ks + r32 * KPITCH + hi * 16;
;     constexpr int R1 = 32 * KPITCH;
;     p0 = f32x16{}; p1 = f32x16{};
;     bf16x8 a0 = k_read<0>(kb), a1 = k_read<R1>(kb), a2 = k_read<32>(kb), a3 = k_read<R1 + 32>(kb), a4 = k_read<64>(kb), a5 = k_read<R1 + 64>(kb);
;     ...
;     QK_STEP(0, a0, a1, 3, 4); QK_STEP(1, a2, a3, 4, 4); QK_STEP(2, a4, a5, 5, 4);
.LBB0_1001:
	s_bitcmp1_b32 s0, 0
	s_cselect_b32 s49, 0x6400, 0
	s_cmp_lg_u32 0, -1
	s_cselect_b32 s0, 0, 0
	s_add_i32 s0, s0, s49
	v_add_u32_e32 v174, s0, v178
	ds_read_b128 v[64:67], v174 offset:0
	ds_read_b128 v[68:71], v174 offset:0x3200
	ds_read_b128 v[180:183], v174 offset:32
	ds_read_b128 v[184:187], v174 offset:0x3220
	ds_read_b128 v[188:191], v174 offset:64
	ds_read_b128 v[192:195], v174 offset:0x3240
	s_nop 0
	s_waitcnt lgkmcnt(4)
	ds_read_b128 v[196:199], v174 offset:0x60
	ds_read_b128 v[200:203], v174 offset:0x3260
	s_waitcnt lgkmcnt(4)
	s_nop 0
	v_mfma_f32_32x32x16_bf16 v[80:95], v[64:67], v[142:145], 0
	v_mfma_f32_32x32x16_bf16 v[64:79], v[68:71], v[142:145], 0
	v_mfma_f32_32x32x16_bf16 v[80:95], v[180:183], v[138:141], v[80:95]
	ds_read_b128 v[180:183], v174 offset:0x80
	v_mfma_f32_32x32x16_bf16 v[64:79], v[184:187], v[138:141], v[64:79]
	ds_read_b128 v[184:187], v174 offset:0x3280
	s_waitcnt lgkmcnt(4)
	s_nop 0
	v_mfma_f32_32x32x16_bf16 v[80:95], v[188:191], v[134:137], v[80:95]
	ds_read_b128 v[188:191], v174 offset:0xa0
	v_mfma_f32_32x32x16_bf16 v[64:79], v[192:195], v[134:137], v[64:79]
	ds_read_b128 v[192:195], v174 offset:0x32a0
	s_waitcnt lgkmcnt(4)
	s_nop 0
	v_mfma_f32_32x32x16_bf16 v[80:95], v[196:199], v[130:133], v[80:95]
	ds_read_b128 v[196:199], v174 offset:0xc0
	v_mfma_f32_32x32x16_bf16 v[64:79], v[200:203], v[130:133], v[64:79]
	ds_read_b128 v[200:203], v174 offset:0x32c0
	s_waitcnt lgkmcnt(4)
	s_nop 0
	v_mfma_f32_32x32x16_bf16 v[80:95], v[180:183], v[126:129], v[80:95]
	ds_read_b128 v[180:183], v174 offset:0xe0
	v_mfma_f32_32x32x16_bf16 v[64:79], v[184:187], v[126:129], v[64:79]
	ds_read_b128 v[184:187], v174 offset:0x32e0
	s_waitcnt lgkmcnt(4)
	s_nop 0
	v_mfma_f32_32x32x16_bf16 v[80:95], v[188:191], v[122:125], v[80:95]
	ds_read_b128 v[188:191], v174 offset:0x100
	v_mfma_f32_32x32x16_bf16 v[64:79], v[192:195], v[122:125], v[64:79]
	ds_read_b128 v[192:195], v174 offset:0x3300
	s_waitcnt lgkmcnt(4)
	s_nop 0
	v_mfma_f32_32x32x16_bf16 v[80:95], v[196:199], v[118:121], v[80:95]
	ds_read_b128 v[196:199], v174 offset:0x120
	v_mfma_f32_32x32x16_bf16 v[64:79], v[200:203], v[118:121], v[64:79]
	ds_read_b128 v[200:203], v174 offset:0x3320
	s_waitcnt lgkmcnt(4)
	s_nop 0
	v_mfma_f32_32x32x16_bf16 v[80:95], v[180:183], v[114:117], v[80:95]
	ds_read_b128 v[180:183], v174 offset:0x140
	v_mfma_f32_32x32x16_bf16 v[64:79], v[184:187], v[114:117], v[64:79]
	ds_read_b128 v[184:187], v174 offset:0x3340
	s_waitcnt lgkmcnt(4)
	s_nop 0
	v_mfma_f32_32x32x16_bf16 v[80:95], v[188:191], v[110:113], v[80:95]
	ds_read_b128 v[188:191], v174 offset:0x160
	v_mfma_f32_32x32x16_bf16 v[64:79], v[192:195], v[110:113], v[64:79]
	ds_read_b128 v[192:195], v174 offset:0x3360
	s_waitcnt lgkmcnt(4)
	s_waitcnt lgkmcnt(2)
	s_nop 0
	s_waitcnt lgkmcnt(0)
	v_add_u32_e32 v207, s49, v172
	ds_read_b64_tr_b16 v[220:221], v207 offset:0
	ds_read_b64_tr_b16 v[222:223], v207 offset:1600
	ds_read_b64_tr_b16 v[224:225], v207 offset:64
	ds_read_b64_tr_b16 v[226:227], v207 offset:1664
	ds_read_b64_tr_b16 v[228:229], v207 offset:128
	ds_read_b64_tr_b16 v[230:231], v207 offset:1728
	ds_read_b64_tr_b16 v[232:233], v207 offset:192
	ds_read_b64_tr_b16 v[234:235], v207 offset:1792
	ds_read_b64_tr_b16 v[236:237], v207 offset:6400
	ds_read_b64_tr_b16 v[238:239], v207 offset:8000
	ds_read_b64_tr_b16 v[240:241], v207 offset:6464
	ds_read_b64_tr_b16 v[242:243], v207 offset:8064
	ds_read_b64_tr_b16 v[244:245], v207 offset:6528
	ds_read_b64_tr_b16 v[246:247], v207 offset:8128
	ds_read_b64_tr_b16 v[248:249], v207 offset:6592
	ds_read_b64_tr_b16 v[250:251], v207 offset:8192
	v_mfma_f32_32x32x16_bf16 v[80:95], v[196:199], v[106:109], v[80:95]
	v_mfma_f32_32x32x16_bf16 v[80:95], v[180:183], v[102:105], v[80:95]
	v_max_f32_e32 v181, v173, v173
	v_mfma_f32_32x32x16_bf16 v[64:79], v[200:203], v[106:109], v[64:79]
	v_mfma_f32_32x32x16_bf16 v[80:95], v[188:191], v[98:101], v[80:95]
	v_mfma_f32_32x32x16_bf16 v[64:79], v[184:187], v[102:105], v[64:79]
	s_nop 10
	v_max_f32_e32 v174, v81, v81
	v_max_f32_e32 v180, v80, v80
	v_max_f32_e32 v174, v180, v174
	v_max3_f32 v174, v174, v82, v83
	v_max3_f32 v174, v174, v84, v85
	v_max3_f32 v174, v174, v86, v87
	v_max3_f32 v174, v174, v88, v89
	v_mfma_f32_32x32x16_bf16 v[64:79], v[192:195], v[98:101], v[64:79]
	v_max3_f32 v174, v174, v90, v91
	v_max3_f32 v174, v174, v92, v93
	v_max3_f32 v174, v174, v94, v95
	s_nop 8
	v_max3_f32 v174, v174, v64, v65
	v_max3_f32 v174, v174, v66, v67
	v_max3_f32 v174, v174, v68, v69
	v_max3_f32 v174, v174, v70, v71
	v_max3_f32 v174, v174, v72, v73
	v_max3_f32 v174, v174, v74, v75
	v_max3_f32 v174, v174, v76, v77
	v_max3_f32 v174, v174, v78, v79
	v_mov_b32_e32 v180, v174
	s_nop 1
	v_permlane32_swap_b32_e32 v174, v180
	v_max_f32_e32 v180, v180, v180
	v_max_f32_e32 v174, v174, v174
	v_max_f32_e32 v174, v174, v180
	v_sub_f32_e32 v180, v174, v173
	v_max_f32_e32 v174, v181, v174
	v_sub_f32_e32 v181, v173, v174
	v_mul_f32_e32 v181, 0x3dd53b94, v181
	v_exp_f32_e32 v181, v181
	v_cmp_ge_f32_e32 vcc, s33, v180
	s_cmp_eq_u64 vcc, exec
	s_cselect_b64 s[38:39], -1, 0
	v_cndmask_b32_e64 v180, v181, 1.0, s[38:39]
	v_cmp_gt_f32_e32 vcc, 1.0, v180
	s_cbranch_vccz .LBB0_1005
	s_and_saveexec_b64 s[0:1], s[36:37]
	ds_write_b32 v171, v180 offset:51328
	s_or_b64 exec, exec, s[0:1]
	s_waitcnt lgkmcnt(0)
	v_add_u32_e32 v181, v159, v96
	ds_read_b128 v[182:185], v181 offset:51424
	ds_read_b128 v[186:189], v181 offset:51392
	ds_read_b128 v[190:193], v181 offset:51360
	ds_read_b128 v[194:197], v181 offset:51328
	s_waitcnt lgkmcnt(3)
	v_pk_mul_f32 v[12:13], v[12:13], v[182:183]
	s_waitcnt lgkmcnt(2)
	v_pk_mul_f32 v[8:9], v[8:9], v[186:187]
	s_waitcnt lgkmcnt(1)
	v_pk_mul_f32 v[4:5], v[4:5], v[190:191]
	v_pk_mul_f32 v[14:15], v[14:15], v[184:185]
	v_pk_mul_f32 v[10:11], v[10:11], v[188:189]
	v_pk_mul_f32 v[6:7], v[6:7], v[192:193]
	s_waitcnt lgkmcnt(0)
	v_pk_mul_f32 v[2:3], v[2:3], v[196:197]
	v_pk_mul_f32 v[0:1], v[0:1], v[194:195]
	v_pk_mul_f32 v[60:61], v[60:61], v[182:183]
	v_pk_mul_f32 v[56:57], v[56:57], v[186:187]
	v_pk_mul_f32 v[52:53], v[52:53], v[190:191]
	v_pk_mul_f32 v[62:63], v[62:63], v[184:185]
	v_pk_mul_f32 v[58:59], v[58:59], v[188:189]
	v_pk_mul_f32 v[54:55], v[54:55], v[192:193]
	v_pk_mul_f32 v[50:51], v[50:51], v[196:197]
	v_pk_mul_f32 v[48:49], v[48:49], v[194:195]
	v_pk_mul_f32 v[44:45], v[44:45], v[182:183]
	v_pk_mul_f32 v[40:41], v[40:41], v[186:187]
	v_pk_mul_f32 v[36:37], v[36:37], v[190:191]
	v_pk_mul_f32 v[46:47], v[46:47], v[184:185]
	v_pk_mul_f32 v[42:43], v[42:43], v[188:189]
	v_pk_mul_f32 v[38:39], v[38:39], v[192:193]
	v_pk_mul_f32 v[34:35], v[34:35], v[196:197]
	v_pk_mul_f32 v[32:33], v[32:33], v[194:195]
	v_pk_mul_f32 v[28:29], v[28:29], v[182:183]
	v_pk_mul_f32 v[24:25], v[24:25], v[186:187]
	v_pk_mul_f32 v[20:21], v[20:21], v[190:191]
	v_pk_mul_f32 v[30:31], v[30:31], v[184:185]
	v_pk_mul_f32 v[26:27], v[26:27], v[188:189]
	v_pk_mul_f32 v[22:23], v[22:23], v[192:193]
	v_pk_mul_f32 v[18:19], v[18:19], v[196:197]
	v_pk_mul_f32 v[16:17], v[16:17], v[194:195]
; #define SBAR() __builtin_amdgcn_sched_barrier(0)
; #define PV_READ(D0, L0, H0, L1, H1, L2, H2, L3, H3) do { L0 = tr_read<v_rd_off(D0, 0, 0)>(vb); H0 = tr_read<v_rd_off(D0, 0, 1)>(vb); L1 = tr_read<v_rd_off(D0, 1, 0)>(vb); H1 = tr_read<v_rd_off(D0, 1, 1)>(vb); \
;     L2 = tr_read<v_rd_off(D0, 2, 0)>(vb); H2 = tr_read<v_rd_off(D0, 2, 1)>(vb); L3 = tr_read<v_rd_off(D0, 3, 0)>(vb); H3 = tr_read<v_rd_off(D0, 3, 1)>(vb); } while (0)
; __device__ __forceinline__ void partialSM(f32x16& p0, f32x16& p1, float& m_reg, float& mn, float& alpha) {
;     ...
;     const float mnC = -mn * C;
; #pragma unroll
;     for (int r = 0; r < 16; ++r) p0[r] = fmaf(p0[r], C, mnC);
; #pragma unroll
;     for (int r = 0; r < 16; ++r) p1[r] = fmaf(p1[r], C, mnC);
; #pragma unroll
;     for (int r = 0; r < 16; ++r) p0[r] = __builtin_amdgcn_exp2f(p0[r]);
; }
; __device__ __forceinline__ void finishSM(f32x16& p0, f32x16& p1, float alpha, float& l_reg, bf16x8& pa0, bf16x8& pa1, bf16x8& pa2, bf16x8& pa3) {
; #pragma unroll
;     for (int r = 0; r < 16; ++r) p1[r] = __builtin_amdgcn_exp2f(p1[r]);
;     float ps = 0;
; #pragma unroll
;     for (int r = 0; r < 16; ++r) ps += p0[r];
; #pragma unroll
;     for (int r = 0; r < 16; ++r) ps += p1[r];
;     { auto rr = __builtin_amdgcn_permlane32_swap(__float_as_uint(ps), __float_as_uint(ps), false, false);
;       ps = __uint_as_float(rr[0]) + __uint_as_float(rr[1]); }
;     l_reg = l_reg * alpha + ps;
;     ...
;     PK4(p0, 0, pa0); PK4(p0, 8, pa1); PK4(p1, 0, pa2); PK4(p1, 8, pa3);
;     ...
; }
; __device__ __forceinline__ void pv_d0(f32x16* o, int vb, bf16x8 pa0, bf16x8 pa1, bf16x8 pa2, bf16x8 pa3) {
;     s16x4 a0, a1, a2, a3, a4, a5, a6, a7, b0, b1, b2, b3, b4, b5, b6, b7;
;     PV_READ(0, a0, a1, a2, a3, a4, a5, a6, a7);
;     PV_READ(1, b0, b1, b2, b3, b4, b5, b6, b7);
;     asm volatile("s_waitcnt lgkmcnt(8)" ::: "memory"); SBAR();
;     PV_MMA(o[0], a0, a1, a2, a3, a4, a5, a6, a7); SBAR();
;     PV_READ(2, a0, a1, a2, a3, a4, a5, a6, a7);
;     asm volatile("s_waitcnt lgkmcnt(8)" ::: "memory"); SBAR();
;     PV_MMA(o[1], b0, b1, b2, b3, b4, b5, b6, b7); SBAR();
;     PV_READ(3, b0, b1, b2, b3, b4, b5, b6, b7);
;     asm volatile("s_waitcnt lgkmcnt(8)" ::: "memory"); SBAR();
;     PV_MMA(o[2], a0, a1, a2, a3, a4, a5, a6, a7); SBAR();
;     asm volatile("s_waitcnt lgkmcnt(0)" ::: "memory"); SBAR();
;     PV_MMA(o[3], b0, b1, b2, b3, b4, b5, b6, b7);
; }
.LBB0_1005:
	v_cndmask_b32_e64 v173, v174, v173, s[38:39]
	v_mul_f32_e32 v174, 0xbdd53b94, v173
	v_mov_b32_e32 v206, v180
	v_fmamk_f32 v80, v80, 0x3dd53b94, v174
	v_fmamk_f32 v81, v81, 0x3dd53b94, v174
	v_fmamk_f32 v82, v82, 0x3dd53b94, v174
	v_fmamk_f32 v83, v83, 0x3dd53b94, v174
	v_fmamk_f32 v84, v84, 0x3dd53b94, v174
	v_fmamk_f32 v85, v85, 0x3dd53b94, v174
	v_fmamk_f32 v86, v86, 0x3dd53b94, v174
	v_fmamk_f32 v87, v87, 0x3dd53b94, v174
	v_exp_f32_e32 v80, v80
	v_exp_f32_e32 v81, v81
	v_exp_f32_e32 v82, v82
	v_exp_f32_e32 v83, v83
	v_exp_f32_e32 v84, v84
	v_exp_f32_e32 v85, v85
	v_exp_f32_e32 v86, v86
	v_exp_f32_e32 v87, v87
	v_add_f32_e32 v204, v80, v81
	v_add_f32_e32 v204, v204, v82
	v_add_f32_e32 v204, v204, v83
	v_add_f32_e32 v204, v204, v84
	v_cvt_pk_bf16_f32 v180, v80, v81
	v_cvt_pk_bf16_f32 v181, v82, v83
	v_cvt_pk_bf16_f32 v182, v84, v85
	v_cvt_pk_bf16_f32 v183, v86, v87
	v_add_f32_e32 v204, v204, v85
	v_add_f32_e32 v204, v204, v86
	v_add_f32_e32 v204, v204, v87
	v_permlane32_swap_b32_e32 v180, v182
	v_permlane32_swap_b32_e32 v181, v183
	s_waitcnt lgkmcnt(8)
	s_nop 1
	v_mfma_f32_32x32x16_bf16 v[0:15], v[180:183], v[220:223], v[0:15]
	v_fmamk_f32 v88, v88, 0x3dd53b94, v174
	v_fmamk_f32 v89, v89, 0x3dd53b94, v174
	v_fmamk_f32 v90, v90, 0x3dd53b94, v174
	v_fmamk_f32 v91, v91, 0x3dd53b94, v174
	v_fmamk_f32 v92, v92, 0x3dd53b94, v174
	v_fmamk_f32 v93, v93, 0x3dd53b94, v174
	v_fmamk_f32 v94, v94, 0x3dd53b94, v174
	v_fmamk_f32 v95, v95, 0x3dd53b94, v174
	v_mfma_f32_32x32x16_bf16 v[48:63], v[180:183], v[224:227], v[48:63]
	v_exp_f32_e32 v88, v88
	v_exp_f32_e32 v89, v89
	v_exp_f32_e32 v90, v90
	v_exp_f32_e32 v91, v91
	v_exp_f32_e32 v92, v92
	v_exp_f32_e32 v93, v93
	v_exp_f32_e32 v94, v94
	v_mfma_f32_32x32x16_bf16 v[32:47], v[180:183], v[228:231], v[32:47]
	v_exp_f32_e32 v95, v95
	v_add_f32_e32 v205, v88, v89
	v_add_f32_e32 v205, v205, v90
	v_add_f32_e32 v205, v205, v91
	v_add_f32_e32 v205, v205, v92
	v_cvt_pk_bf16_f32 v184, v88, v89
	v_cvt_pk_bf16_f32 v185, v90, v91
	v_mfma_f32_32x32x16_bf16 v[16:31], v[180:183], v[232:235], v[16:31]
	v_cvt_pk_bf16_f32 v186, v92, v93
	v_cvt_pk_bf16_f32 v187, v94, v95
	v_add_f32_e32 v205, v205, v93
	v_add_f32_e32 v205, v205, v94
	v_add_f32_e32 v205, v205, v95
	v_permlane32_swap_b32_e32 v184, v186
	v_permlane32_swap_b32_e32 v185, v187
	ds_read_b64_tr_b16 v[220:221], v207 offset:12800
	ds_read_b64_tr_b16 v[222:223], v207 offset:14400
	ds_read_b64_tr_b16 v[224:225], v207 offset:12864
	ds_read_b64_tr_b16 v[226:227], v207 offset:14464
	ds_read_b64_tr_b16 v[228:229], v207 offset:12928
	ds_read_b64_tr_b16 v[230:231], v207 offset:14528
	ds_read_b64_tr_b16 v[232:233], v207 offset:12992
	ds_read_b64_tr_b16 v[234:235], v207 offset:14592
	s_waitcnt lgkmcnt(8)
	v_mfma_f32_32x32x16_bf16 v[0:15], v[184:187], v[236:239], v[0:15]
	v_fmamk_f32 v64, v64, 0x3dd53b94, v174
	v_fmamk_f32 v65, v65, 0x3dd53b94, v174
	v_fmamk_f32 v66, v66, 0x3dd53b94, v174
	v_fmamk_f32 v67, v67, 0x3dd53b94, v174
	v_fmamk_f32 v68, v68, 0x3dd53b94, v174
	v_fmamk_f32 v69, v69, 0x3dd53b94, v174
	v_fmamk_f32 v70, v70, 0x3dd53b94, v174
	v_fmamk_f32 v71, v71, 0x3dd53b94, v174
	v_mfma_f32_32x32x16_bf16 v[48:63], v[184:187], v[240:243], v[48:63]
	v_exp_f32_e32 v64, v64
	v_exp_f32_e32 v65, v65
	v_exp_f32_e32 v66, v66
	v_exp_f32_e32 v67, v67
	v_exp_f32_e32 v68, v68
	v_exp_f32_e32 v69, v69
	v_exp_f32_e32 v70, v70
	v_exp_f32_e32 v71, v71
	v_mfma_f32_32x32x16_bf16 v[32:47], v[184:187], v[244:247], v[32:47]
	v_add_f32_e32 v204, v204, v64
	v_add_f32_e32 v204, v204, v65
	v_add_f32_e32 v204, v204, v66
	v_add_f32_e32 v204, v204, v67
	v_cvt_pk_bf16_f32 v188, v64, v65
	v_cvt_pk_bf16_f32 v189, v66, v67
	v_cvt_pk_bf16_f32 v190, v68, v69
	v_mfma_f32_32x32x16_bf16 v[16:31], v[184:187], v[248:251], v[16:31]
	v_cvt_pk_bf16_f32 v191, v70, v71
	v_add_f32_e32 v204, v204, v68
	v_add_f32_e32 v204, v204, v69
	v_add_f32_e32 v204, v204, v70
	v_add_f32_e32 v204, v204, v71
	v_permlane32_swap_b32_e32 v188, v190
	v_permlane32_swap_b32_e32 v189, v191
	ds_read_b64_tr_b16 v[236:237], v207 offset:19200
	ds_read_b64_tr_b16 v[238:239], v207 offset:20800
	ds_read_b64_tr_b16 v[240:241], v207 offset:19264
	ds_read_b64_tr_b16 v[242:243], v207 offset:20864
	ds_read_b64_tr_b16 v[244:245], v207 offset:19328
	ds_read_b64_tr_b16 v[246:247], v207 offset:20928
	ds_read_b64_tr_b16 v[248:249], v207 offset:19392
	ds_read_b64_tr_b16 v[250:251], v207 offset:20992
	s_waitcnt lgkmcnt(8)
	v_mfma_f32_32x32x16_bf16 v[0:15], v[188:191], v[220:223], v[0:15]
	v_fmamk_f32 v72, v72, 0x3dd53b94, v174
	v_fmamk_f32 v73, v73, 0x3dd53b94, v174
	v_fmamk_f32 v74, v74, 0x3dd53b94, v174
	v_fmamk_f32 v75, v75, 0x3dd53b94, v174
	v_fmamk_f32 v76, v76, 0x3dd53b94, v174
	v_fmamk_f32 v77, v77, 0x3dd53b94, v174
	v_fmamk_f32 v78, v78, 0x3dd53b94, v174
	v_fmamk_f32 v79, v79, 0x3dd53b94, v174
	v_mfma_f32_32x32x16_bf16 v[48:63], v[188:191], v[224:227], v[48:63]
	v_exp_f32_e32 v72, v72
	v_exp_f32_e32 v73, v73
	v_exp_f32_e32 v74, v74
	v_exp_f32_e32 v75, v75
	v_exp_f32_e32 v76, v76
	v_exp_f32_e32 v77, v77
	v_exp_f32_e32 v78, v78
	v_exp_f32_e32 v79, v79
	v_mfma_f32_32x32x16_bf16 v[32:47], v[188:191], v[228:231], v[32:47]
	v_add_f32_e32 v205, v205, v72
	v_add_f32_e32 v205, v205, v73
	v_add_f32_e32 v205, v205, v74
	v_add_f32_e32 v205, v205, v75
	v_cvt_pk_bf16_f32 v192, v72, v73
	v_cvt_pk_bf16_f32 v193, v74, v75
	v_cvt_pk_bf16_f32 v194, v76, v77
	v_mfma_f32_32x32x16_bf16 v[16:31], v[188:191], v[232:235], v[16:31]
	v_cvt_pk_bf16_f32 v195, v78, v79
	v_add_f32_e32 v205, v205, v76
	v_add_f32_e32 v205, v205, v77
	v_add_f32_e32 v205, v205, v78
	v_add_f32_e32 v205, v205, v79
	v_permlane32_swap_b32_e32 v192, v194
	v_permlane32_swap_b32_e32 v193, v195
	s_waitcnt lgkmcnt(0)
	s_nop 1
	v_mfma_f32_32x32x16_bf16 v[0:15], v[192:195], v[236:239], v[0:15]
	v_add_f32_e32 v204, v204, v205
	v_mov_b32_e32 v205, v204
	v_mfma_f32_32x32x16_bf16 v[48:63], v[192:195], v[240:243], v[48:63]
	s_nop 1
	v_permlane32_swap_b32_e32 v204, v205
	v_mfma_f32_32x32x16_bf16 v[32:47], v[192:195], v[244:247], v[32:47]
	v_add_f32_e32 v174, v204, v205
	v_mfma_f32_32x32x16_bf16 v[16:31], v[192:195], v[248:251], v[16:31]
	v_fmac_f32_e32 v174, v179, v206
	s_add_u32 s2, s2, 0x6000
	s_addc_u32 s3, s3, 0
	s_cmp_eq_u32 s2, 0x17a000
	s_cbranch_scc1 .LBB0_1007
	s_mov_b32 s0, s29
	v_mov_b32_e32 v179, v174
	s_branch .LBB0_999

; #define PG8_STAGE(bufoff, gbase, voff) do { _Pragma("unroll") for (int _i = 0; _i < 2; ++_i) \
;         __builtin_amdgcn_global_load_lds((const __attribute__((address_space(1))) unsigned*)((const __attribute__((address_space(1))) char*)(gbase) + (unsigned)lnd_v((int)(voff)[_i])), (LAS unsigned*)(lds + (bufoff) + ldsw + _i * 8192), 16, 0, 0); } while (0)
; #define PG8_WAIT_V(n) asm volatile("s_waitcnt vmcnt(" #n ")" ::: "memory")
; #define PG8_BAR __builtin_amdgcn_s_barrier()
; template <class Desc, class Epi>
; __device__ __forceinline__ void gemm_phase(const int wv_, LAS unsigned char* lds, const Desc& d, const Epi& E) {
;     ...
;     const unsigned ldsw = (unsigned)wid * 1024u;
;     const int aoff = lds_byte(wr * 64 + fr, fq * 8), boff = lds_byte(wc * 32 + fr, fq * 8);
;     ...
;     const char* cA = (const char*)cur.a; const char* cB = (const char*)cur.b;
;     PG8_STAGE(PG8_SB(0, 0), cB, voffB); PG8_STAGE(PG8_SB(0, 1), cB + hstepB, voffB); PG8_STAGE(PG8_SA(0, 0), cA, voffA); PG8_STAGE(PG8_SA(0, 1), cA, voffA1);
;     if (wr == 1) PG8_BAR;
;     PG8_WAIT_V(2); PG8_BAR;
;     PG8_STAGE(PG8_SB(1, 0), cB + kstep, voffB); PG8_STAGE(PG8_SA(1, 0), cA + kstep, voffA); PG8_STAGE(PG8_SB(1, 1), cB + hstepB + kstep, voffB);
;     PG8_WAIT_V(6); PG8_BAR;
.LBB0_1069:
	s_lshr_b32 s0, s0, 2
	s_add_u32 s40, s20, 0x33600000
	s_addc_u32 s41, s21, 0
	v_bfe_u32 v2, v0, 4, 2
	s_add_u32 s42, s20, 0x37800000
	v_and_b32_e32 v1, 15, v0
	v_lshlrev_b32_e32 v4, 4, v2
	v_lshlrev_b32_e32 v0, 2, v0
	s_addc_u32 s43, s21, 0
	s_and_b32 s65, s26, 3
	v_lshl_or_b32 v225, s29, 6, v1
	v_lshl_or_b32 v1, v1, 6, v4
	s_lshl_b32 s20, s29, 13
	v_and_b32_e32 v0, 32, v0
	v_bitop3_b32 v4, v1, s20, v0 bitop3:0xde
	s_lshl_b32 s20, s65, 12
	v_mov_b32_e32 v96, v221
	v_bitop3_b32 v226, v1, s20, v0 bitop3:0xde
	s_waitcnt vmcnt(2)
	s_barrier
	s_add_i32 m0, s60, 0x18000
	v_lshl_add_u64 v[0:1], s[4:5], 0, v[96:97]
	v_lshl_add_u64 v[0:1], v[0:1], 0, s[30:31]
	v_mov_b32_e32 v96, v224
	global_load_lds_dwordx4 v[0:1], off
	s_add_i32 m0, s60, 0x1a000
	v_lshl_add_u64 v[0:1], s[4:5], 0, v[96:97]
	v_lshl_add_u64 v[0:1], v[0:1], 0, s[30:31]
	v_mov_b32_e32 v96, v219
	global_load_lds_dwordx4 v[0:1], off
	s_add_i32 s66, s60, 0x8000
	v_lshl_add_u64 v[0:1], s[2:3], 0, v[96:97]
	v_lshl_add_u64 v[0:1], v[0:1], 0, s[30:31]
	s_mov_b32 m0, s66
	v_mov_b32_e32 v96, v222
	global_load_lds_dwordx4 v[0:1], off
	s_add_i32 s67, s60, 0xa000
	v_lshl_add_u64 v[0:1], s[2:3], 0, v[96:97]
	v_lshl_add_u64 v[0:1], v[0:1], 0, s[30:31]
	s_mov_b32 m0, s67
	s_add_u32 s20, s4, 0x40080
	global_load_lds_dwordx4 v[0:1], off
	v_mov_b32_e32 v0, v221
	s_addc_u32 s21, s5, 0
	s_add_i32 m0, s60, 0x1c000
	v_lshlrev_b32_e32 v3, 3, v2
	global_load_lds_dwordx4 v0, s[20:21]
	v_mov_b32_e32 v0, v224
	s_add_i32 m0, s60, 0x1e000
	s_cmpk_lt_u32 s1, 0x100
	global_load_lds_dwordx4 v0, s[20:21]
	s_waitcnt vmcnt(6)
	s_cselect_b64 s[44:45], -1, 0
	v_lshl_or_b32 v227, s65, 5, v3
	s_mov_b32 s68, 0
	v_cmp_eq_u32_e64 s[36:37], 0, v2
	v_or_b32_e32 v228, 16, v225
	v_or_b32_e32 v229, 32, v225
	v_or_b32_e32 v230, 48, v225
	v_add_u32_e32 v231, 0, v4
	s_mov_b64 s[52:53], s[4:5]
	s_mov_b64 s[50:51], s[2:3]
	s_barrier
	s_waitcnt vmcnt(0)
	s_branch .LBB0_1072

; template <class Desc, class Epi>
; __device__ __forceinline__ void gemm_phase(const int wv_, LAS unsigned char* lds, const Desc& d, const Epi& E) {
;     ...
; #pragma unroll
;         for (int a = 0; a < 2; ++a)
; #pragma unroll
;             for (int b = 0; b < 2; ++b)
; #pragma unroll
;                 for (int m = 0; m < 4; ++m)
; #pragma unroll
;                     for (int n = 0; n < 2; ++n) acc[a][b][m][n] = (f32x4){0.f, 0.f, 0.f, 0.f};
;         cur = nxt; cA = nA; cB = nB; ++ui;
;         if constexpr (Desc::GATHER) { voffA[0] = voffAn[0]; voffA[1] = voffAn[1]; voffA1[0] = voffAn1[0]; voffA1[1] = voffAn1[1]; }
.LBB0_1074:
	s_add_u32 s2, s2, 0x80
	s_addc_u32 s3, s3, 0
	s_add_u32 s1, s4, 0x100
	v_mov_b32_e32 v32, 0
	s_addc_u32 s26, s5, 0
	s_mov_b32 s29, -2
	v_mov_b32_e32 v33, v32
	v_mov_b32_e32 v34, v32
	v_mov_b32_e32 v35, v32
	v_mov_b32_e32 v36, v32
	v_mov_b32_e32 v37, v32
	v_mov_b32_e32 v38, v32
	v_mov_b32_e32 v39, v32
	v_mov_b32_e32 v48, v32
	v_mov_b32_e32 v49, v32
	v_mov_b32_e32 v50, v32
	v_mov_b32_e32 v51, v32
	v_mov_b32_e32 v52, v32
	v_mov_b32_e32 v53, v32
	v_mov_b32_e32 v54, v32
	v_mov_b32_e32 v55, v32
	v_mov_b32_e32 v0, v32
	v_mov_b32_e32 v1, v32
	v_mov_b32_e32 v2, v32
	v_mov_b32_e32 v3, v32
	v_mov_b32_e32 v4, v32
	v_mov_b32_e32 v5, v32
	v_mov_b32_e32 v6, v32
	v_mov_b32_e32 v7, v32
	v_mov_b32_e32 v16, v32
	v_mov_b32_e32 v17, v32
	v_mov_b32_e32 v18, v32
	v_mov_b32_e32 v19, v32
	v_mov_b32_e32 v20, v32
	v_mov_b32_e32 v21, v32
	v_mov_b32_e32 v22, v32
	v_mov_b32_e32 v23, v32
	v_mov_b32_e32 v40, v32
	v_mov_b32_e32 v41, v32
	v_mov_b32_e32 v42, v32
	v_mov_b32_e32 v43, v32
	v_mov_b32_e32 v44, v32
	v_mov_b32_e32 v45, v32
	v_mov_b32_e32 v46, v32
	v_mov_b32_e32 v47, v32
	v_mov_b32_e32 v56, v32
	v_mov_b32_e32 v57, v32
	v_mov_b32_e32 v58, v32
	v_mov_b32_e32 v59, v32
	v_mov_b32_e32 v60, v32
	v_mov_b32_e32 v61, v32
	v_mov_b32_e32 v62, v32
	v_mov_b32_e32 v63, v32
	v_mov_b32_e32 v64, v32
	v_mov_b32_e32 v65, v32
	v_mov_b32_e32 v66, v32
	v_mov_b32_e32 v67, v32
	v_mov_b32_e32 v68, v32
	v_mov_b32_e32 v69, v32
	v_mov_b32_e32 v70, v32
	v_mov_b32_e32 v71, v32
	v_mov_b32_e32 v80, v32
	v_mov_b32_e32 v81, v32
	v_mov_b32_e32 v82, v32
	v_mov_b32_e32 v83, v32
	v_mov_b32_e32 v84, v32
	v_mov_b32_e32 v85, v32
	v_mov_b32_e32 v86, v32
	v_mov_b32_e32 v87, v32
	v_mov_b32_e32 v98, v32
	v_mov_b32_e32 v99, v32
	v_mov_b32_e32 v100, v32
	v_mov_b32_e32 v101, v32
	v_mov_b32_e32 v102, v32
	v_mov_b32_e32 v103, v32
	v_mov_b32_e32 v104, v32
	v_mov_b32_e32 v105, v32
	v_mov_b32_e32 v114, v32
	v_mov_b32_e32 v115, v32
	v_mov_b32_e32 v116, v32
	v_mov_b32_e32 v117, v32
	v_mov_b32_e32 v122, v32
	v_mov_b32_e32 v123, v32
	v_mov_b32_e32 v124, v32
	v_mov_b32_e32 v125, v32
	v_mov_b32_e32 v72, v32
	v_mov_b32_e32 v73, v32
	v_mov_b32_e32 v74, v32
	v_mov_b32_e32 v75, v32
	v_mov_b32_e32 v76, v32
	v_mov_b32_e32 v77, v32
	v_mov_b32_e32 v78, v32
	v_mov_b32_e32 v79, v32
	v_mov_b32_e32 v88, v32
	v_mov_b32_e32 v89, v32
	v_mov_b32_e32 v90, v32
	v_mov_b32_e32 v91, v32
	v_mov_b32_e32 v92, v32
	v_mov_b32_e32 v93, v32
	v_mov_b32_e32 v94, v32
	v_mov_b32_e32 v95, v32
	v_mov_b32_e32 v106, v32
	v_mov_b32_e32 v107, v32
	v_mov_b32_e32 v108, v32
	v_mov_b32_e32 v109, v32
	v_mov_b32_e32 v110, v32
	v_mov_b32_e32 v111, v32
	v_mov_b32_e32 v112, v32
	v_mov_b32_e32 v113, v32
	v_mov_b32_e32 v138, v32
	v_mov_b32_e32 v139, v32
	v_mov_b32_e32 v140, v32
	v_mov_b32_e32 v141, v32
	v_mov_b32_e32 v146, v32
	v_mov_b32_e32 v147, v32
	v_mov_b32_e32 v148, v32
	v_mov_b32_e32 v149, v32
	v_mov_b32_e32 v28, v32
	v_mov_b32_e32 v29, v32
	v_mov_b32_e32 v30, v32
	v_mov_b32_e32 v31, v32
	v_mov_b32_e32 v24, v32
	v_mov_b32_e32 v25, v32
	v_mov_b32_e32 v26, v32
	v_mov_b32_e32 v27, v32
	v_mov_b32_e32 v12, v32
	v_mov_b32_e32 v13, v32
	v_mov_b32_e32 v14, v32
	v_mov_b32_e32 v15, v32
	v_mov_b32_e32 v8, v32
	v_mov_b32_e32 v9, v32
	v_mov_b32_e32 v10, v32
	v_mov_b32_e32 v11, v32

; #define PG8_STAGE(bufoff, gbase, voff) do { _Pragma("unroll") for (int _i = 0; _i < 2; ++_i) \
;         __builtin_amdgcn_global_load_lds((const __attribute__((address_space(1))) unsigned*)((const __attribute__((address_space(1))) char*)(gbase) + (unsigned)lnd_v((int)(voff)[_i])), (LAS unsigned*)(lds + (bufoff) + ldsw + _i * 8192), 16, 0, 0); } while (0)
; #define PG8_WAIT_V(n) asm volatile("s_waitcnt vmcnt(" #n ")" ::: "memory")
; #define PG8_BAR __builtin_amdgcn_s_barrier()
; template <class Desc, class Epi>
; __device__ __forceinline__ void gemm_phase(const int wv_, LAS unsigned char* lds, const Desc& d, const Epi& E) {
;     ...
;     const unsigned ldsw = (unsigned)wid * 1024u;
;     const int aoff = lds_byte(wr * 64 + fr, fq * 8), boff = lds_byte(wc * 32 + fr, fq * 8);
;     ...
;     const char* cA = (const char*)cur.a; const char* cB = (const char*)cur.b;
;     PG8_STAGE(PG8_SB(0, 0), cB, voffB); PG8_STAGE(PG8_SB(0, 1), cB + hstepB, voffB); PG8_STAGE(PG8_SA(0, 0), cA, voffA); PG8_STAGE(PG8_SA(0, 1), cA, voffA1);
;     if (wr == 1) PG8_BAR;
;     PG8_WAIT_V(2); PG8_BAR;
;     PG8_STAGE(PG8_SB(1, 0), cB + kstep, voffB); PG8_STAGE(PG8_SA(1, 0), cA + kstep, voffA); PG8_STAGE(PG8_SB(1, 1), cB + hstepB + kstep, voffB);
;     PG8_WAIT_V(6); PG8_BAR;
.LBB0_1155:
	s_lshr_b32 s64, s36, 2
	v_mov_b32_e32 v96, v192
	s_add_u32 s40, s2, 0x61400000
	s_waitcnt vmcnt(2)
	s_barrier
	s_addc_u32 s41, s0, 0
	v_lshl_add_u64 v[2:3], s[4:5], 0, v[96:97]
	s_add_i32 m0, s55, 0x18000
	v_lshl_add_u64 v[2:3], v[2:3], 0, s[30:31]
	v_mov_b32_e32 v96, v195
	global_load_lds_dwordx4 v[2:3], off
	s_add_i32 m0, s55, 0x1a000
	v_lshl_add_u64 v[2:3], s[4:5], 0, v[96:97]
	v_lshl_add_u64 v[2:3], v[2:3], 0, s[30:31]
	v_mov_b32_e32 v96, v190
	global_load_lds_dwordx4 v[2:3], off
	s_add_i32 s59, s55, 0x8000
	v_lshl_add_u64 v[2:3], s[20:21], 0, v[96:97]
	s_and_b32 s2, s29, 3
	v_lshl_add_u64 v[2:3], v[2:3], 0, s[30:31]
	s_mov_b32 m0, s59
	v_mov_b32_e32 v96, v193
	s_lshl_b32 s0, s3, 13
	s_lshl_b32 s29, s2, 12
	global_load_lds_dwordx4 v[2:3], off
	s_add_i32 s60, s55, 0xa000
	v_lshl_add_u64 v[2:3], s[20:21], 0, v[96:97]
	v_lshl_add_u64 v[2:3], v[2:3], 0, s[30:31]
	s_mov_b32 m0, s60
	s_add_u32 s36, s4, 0x40080
	v_mov_b32_e32 v1, v192
	global_load_lds_dwordx4 v[2:3], off
	s_addc_u32 s37, s5, 0
	s_add_i32 m0, s55, 0x1c000
	v_bfe_u32 v2, v0, 4, 2
	global_load_lds_dwordx4 v1, s[36:37]
	v_mov_b32_e32 v1, v195
	s_add_i32 m0, s55, 0x1e000
	v_lshlrev_b32_e32 v4, 4, v2
	global_load_lds_dwordx4 v1, s[36:37]
	v_and_b32_e32 v1, 15, v0
	v_lshlrev_b32_e32 v0, 2, v0
	s_cmpk_lt_u32 s1, 0x100
	v_lshl_or_b32 v196, s3, 6, v1
	v_lshl_or_b32 v4, v1, 6, v4
	v_and_b32_e32 v0, 32, v0
	s_cselect_b64 s[42:43], -1, 0
	s_and_b32 s1, s1, 0x3fffff00
	v_lshlrev_b32_e32 v3, 3, v2
	v_lshlrev_b32_e32 v5, 2, v196
	v_bitop3_b32 v197, v4, s29, v0 bitop3:0xde
	v_readlane_b32 s29, v254, 54
	s_lshl_b32 s1, s1, 2
	v_and_b32_e32 v6, 32, v5
	s_waitcnt vmcnt(6)
	v_lshl_or_b32 v198, s2, 5, v3
	v_or_b32_e32 v200, 16, v196
	v_or_b32_e32 v202, 32, v196
	v_or_b32_e32 v204, 48, v196
	v_add_u32_e32 v206, 0x80, v196
	v_add_u32_e32 v208, 0x90, v196
	v_add_u32_e32 v210, 0xa0, v196
	v_add_u32_e32 v212, 0xb0, v196
	s_lshl_b32 s2, s2, 2
	s_add_i32 s1, s29, s1
	v_bitop3_b32 v6, v4, s0, v6 bitop3:0xde
	v_lshlrev_b32_e32 v199, 4, v196
	v_lshlrev_b32_e32 v201, 4, v200
	v_lshlrev_b32_e32 v203, 4, v202
	v_lshlrev_b32_e32 v205, 4, v204
	v_lshlrev_b32_e32 v207, 4, v206
	v_lshlrev_b32_e32 v209, 4, v208
	v_lshlrev_b32_e32 v211, 4, v210
	v_lshlrev_b32_e32 v213, 4, v212
	s_add_i32 s3, s2, s29
	v_lshl_add_u32 v225, v1, 4, s1
	s_add_i32 s1, 0, 0x20000
	s_mov_b32 s0, 0
	v_cmp_eq_u32_e64 s[36:37], 0, v2
	v_add_u32_e32 v214, s3, v199
	v_add_u32_e32 v215, s3, v201
	v_add_u32_e32 v219, s3, v203
	v_add_u32_e32 v220, s3, v205
	v_add_u32_e32 v221, s3, v207
	v_add_u32_e32 v222, s3, v209
	v_add_u32_e32 v223, s3, v211
	v_add_u32_e32 v224, s3, v213
	v_add_u32_e32 v226, s2, v225
	v_add_u32_e32 v227, s1, v5
	v_add_u32_e32 v228, 0, v6
	s_mov_b64 s[48:49], s[4:5]
	s_mov_b64 s[46:47], s[20:21]
	s_barrier
	s_waitcnt vmcnt(0)
	s_branch .LBB0_1158

; template <class Desc, class Epi>
; __device__ __forceinline__ void gemm_phase(const int wv_, LAS unsigned char* lds, const Desc& d, const Epi& E) {
;     ...
; #pragma unroll
;         for (int a = 0; a < 2; ++a)
; #pragma unroll
;             for (int b = 0; b < 2; ++b)
; #pragma unroll
;                 for (int m = 0; m < 4; ++m)
; #pragma unroll
;                     for (int n = 0; n < 2; ++n) acc[a][b][m][n] = (f32x4){0.f, 0.f, 0.f, 0.f};
;         cur = nxt; cA = nA; cB = nB; ++ui;
;         if constexpr (Desc::GATHER) { voffA[0] = voffAn[0]; voffA[1] = voffAn[1]; voffA1[0] = voffAn1[0]; voffA1[1] = voffAn1[1]; }
.LBB0_1160:
	s_add_u32 s2, s20, 0x80
	s_addc_u32 s3, s21, 0
	s_add_u32 s1, s4, 0x100
	v_mov_b32_e32 v12, 0
	s_addc_u32 s29, s5, 0
	s_mov_b32 s45, -2
	v_mov_b32_e32 v13, v12
	v_mov_b32_e32 v14, v12
	v_mov_b32_e32 v15, v12
	v_mov_b32_e32 v20, v12
	v_mov_b32_e32 v21, v12
	v_mov_b32_e32 v22, v12
	v_mov_b32_e32 v23, v12
	v_mov_b32_e32 v36, v12
	v_mov_b32_e32 v37, v12
	v_mov_b32_e32 v38, v12
	v_mov_b32_e32 v39, v12
	v_mov_b32_e32 v44, v12
	v_mov_b32_e32 v45, v12
	v_mov_b32_e32 v46, v12
	v_mov_b32_e32 v47, v12
	v_mov_b32_e32 v0, v12
	v_mov_b32_e32 v1, v12
	v_mov_b32_e32 v2, v12
	v_mov_b32_e32 v3, v12
	v_mov_b32_e32 v4, v12
	v_mov_b32_e32 v5, v12
	v_mov_b32_e32 v6, v12
	v_mov_b32_e32 v7, v12
	v_mov_b32_e32 v8, v12
	v_mov_b32_e32 v9, v12
	v_mov_b32_e32 v10, v12
	v_mov_b32_e32 v11, v12
	v_mov_b32_e32 v16, v12
	v_mov_b32_e32 v17, v12
	v_mov_b32_e32 v18, v12
	v_mov_b32_e32 v19, v12
	v_mov_b32_e32 v32, v12
	v_mov_b32_e32 v33, v12
	v_mov_b32_e32 v34, v12
	v_mov_b32_e32 v35, v12
	v_mov_b32_e32 v40, v12
	v_mov_b32_e32 v41, v12
	v_mov_b32_e32 v42, v12
	v_mov_b32_e32 v43, v12
	v_mov_b32_e32 v56, v12
	v_mov_b32_e32 v57, v12
	v_mov_b32_e32 v58, v12
	v_mov_b32_e32 v59, v12
	v_mov_b32_e32 v60, v12
	v_mov_b32_e32 v61, v12
	v_mov_b32_e32 v62, v12
	v_mov_b32_e32 v63, v12
	v_mov_b32_e32 v64, v12
	v_mov_b32_e32 v65, v12
	v_mov_b32_e32 v66, v12
	v_mov_b32_e32 v67, v12
	v_mov_b32_e32 v68, v12
	v_mov_b32_e32 v69, v12
	v_mov_b32_e32 v70, v12
	v_mov_b32_e32 v71, v12
	v_mov_b32_e32 v76, v12
	v_mov_b32_e32 v77, v12
	v_mov_b32_e32 v78, v12
	v_mov_b32_e32 v79, v12
	v_mov_b32_e32 v84, v12
	v_mov_b32_e32 v85, v12
	v_mov_b32_e32 v86, v12
	v_mov_b32_e32 v87, v12
	v_mov_b32_e32 v92, v12
	v_mov_b32_e32 v93, v12
	v_mov_b32_e32 v94, v12
	v_mov_b32_e32 v95, v12
	v_mov_b32_e32 v102, v12
	v_mov_b32_e32 v103, v12
	v_mov_b32_e32 v104, v12
	v_mov_b32_e32 v105, v12
	v_mov_b32_e32 v110, v12
	v_mov_b32_e32 v111, v12
	v_mov_b32_e32 v112, v12
	v_mov_b32_e32 v113, v12
	v_mov_b32_e32 v118, v12
	v_mov_b32_e32 v119, v12
	v_mov_b32_e32 v120, v12
	v_mov_b32_e32 v121, v12
	v_mov_b32_e32 v72, v12
	v_mov_b32_e32 v73, v12
	v_mov_b32_e32 v74, v12
	v_mov_b32_e32 v75, v12
	v_mov_b32_e32 v80, v12
	v_mov_b32_e32 v81, v12
	v_mov_b32_e32 v82, v12
	v_mov_b32_e32 v83, v12
	v_mov_b32_e32 v88, v12
	v_mov_b32_e32 v89, v12
	v_mov_b32_e32 v90, v12
	v_mov_b32_e32 v91, v12
	v_mov_b32_e32 v98, v12
	v_mov_b32_e32 v99, v12
	v_mov_b32_e32 v100, v12
	v_mov_b32_e32 v101, v12
	v_mov_b32_e32 v106, v12
	v_mov_b32_e32 v107, v12
	v_mov_b32_e32 v108, v12
	v_mov_b32_e32 v109, v12
	v_mov_b32_e32 v114, v12
	v_mov_b32_e32 v115, v12
	v_mov_b32_e32 v116, v12
	v_mov_b32_e32 v117, v12
	v_mov_b32_e32 v122, v12
	v_mov_b32_e32 v123, v12
	v_mov_b32_e32 v124, v12
	v_mov_b32_e32 v125, v12
	v_mov_b32_e32 v126, v12
	v_mov_b32_e32 v127, v12
	v_mov_b32_e32 v128, v12
	v_mov_b32_e32 v129, v12
	v_mov_b32_e32 v52, v12
	v_mov_b32_e32 v53, v12
	v_mov_b32_e32 v54, v12
	v_mov_b32_e32 v55, v12
	v_mov_b32_e32 v48, v12
	v_mov_b32_e32 v49, v12
	v_mov_b32_e32 v50, v12
	v_mov_b32_e32 v51, v12
	v_mov_b32_e32 v28, v12
	v_mov_b32_e32 v29, v12
	v_mov_b32_e32 v30, v12
	v_mov_b32_e32 v31, v12
	v_mov_b32_e32 v24, v12
	v_mov_b32_e32 v25, v12
	v_mov_b32_e32 v26, v12
	v_mov_b32_e32 v27, v12

; #define PG8_STAGE(bufoff, gbase, voff) do { _Pragma("unroll") for (int _i = 0; _i < 2; ++_i) \
;         __builtin_amdgcn_global_load_lds((const __attribute__((address_space(1))) unsigned*)((const __attribute__((address_space(1))) char*)(gbase) + (unsigned)lnd_v((int)(voff)[_i])), (LAS unsigned*)(lds + (bufoff) + ldsw + _i * 8192), 16, 0, 0); } while (0)
; #define PG8_WAIT_V(n) asm volatile("s_waitcnt vmcnt(" #n ")" ::: "memory")
; #define PG8_BAR __builtin_amdgcn_s_barrier()
; template <class Desc, class Epi>
; __device__ __forceinline__ void gemm_phase(const int wv_, LAS unsigned char* lds, const Desc& d, const Epi& E) {
;     ...
;     const unsigned ldsw = (unsigned)wid * 1024u;
;     const int aoff = lds_byte(wr * 64 + fr, fq * 8), boff = lds_byte(wc * 32 + fr, fq * 8);
;     ...
;     const char* cA = (const char*)cur.a; const char* cB = (const char*)cur.b;
;     PG8_STAGE(PG8_SB(0, 0), cB, voffB); PG8_STAGE(PG8_SB(0, 1), cB + hstepB, voffB); PG8_STAGE(PG8_SA(0, 0), cA, voffA); PG8_STAGE(PG8_SA(0, 1), cA, voffA1);
;     if (wr == 1) PG8_BAR;
;     PG8_WAIT_V(2); PG8_BAR;
;     PG8_STAGE(PG8_SB(1, 0), cB + kstep, voffB); PG8_STAGE(PG8_SA(1, 0), cA + kstep, voffA); PG8_STAGE(PG8_SB(1, 1), cB + hstepB + kstep, voffB);
;     PG8_WAIT_V(6); PG8_BAR;
.LBB0_1256:
	s_lshr_b32 s1, s1, 2
	v_mov_b32_e32 v96, v208
	s_add_u32 s38, s20, 0x33600000
	s_waitcnt vmcnt(2)
	s_barrier
	s_addc_u32 s39, s21, 0
	v_lshl_add_u64 v[2:3], s[4:5], 0, v[96:97]
	s_add_i32 m0, s53, 0x18000
	v_lshl_add_u64 v[2:3], v[2:3], 0, s[30:31]
	v_mov_b32_e32 v96, v211
	global_load_lds_dwordx4 v[2:3], off
	s_add_i32 m0, s53, 0x1a000
	v_lshl_add_u64 v[2:3], s[4:5], 0, v[96:97]
	v_lshl_add_u64 v[2:3], v[2:3], 0, s[30:31]
	v_mov_b32_e32 v96, v206
	global_load_lds_dwordx4 v[2:3], off
	s_add_i32 s57, s53, 0x8000
	v_lshl_add_u64 v[2:3], s[2:3], 0, v[96:97]
	s_and_b32 s42, s41, 3
	v_lshl_add_u64 v[2:3], v[2:3], 0, s[30:31]
	s_mov_b32 m0, s57
	v_mov_b32_e32 v96, v209
	s_lshl_b32 s41, s40, 13
	s_lshl_b32 s43, s42, 12
	global_load_lds_dwordx4 v[2:3], off
	s_add_i32 s58, s53, 0xa000
	v_lshl_add_u64 v[2:3], s[2:3], 0, v[96:97]
	v_lshl_add_u64 v[2:3], v[2:3], 0, s[30:31]
	s_mov_b32 m0, s58
	s_add_u32 s20, s4, 0x40080
	v_mov_b32_e32 v1, v208
	global_load_lds_dwordx4 v[2:3], off
	s_addc_u32 s21, s5, 0
	s_add_i32 m0, s53, 0x1c000
	v_bfe_u32 v2, v0, 4, 2
	global_load_lds_dwordx4 v1, s[20:21]
	v_mov_b32_e32 v1, v211
	s_add_i32 m0, s53, 0x1e000
	v_lshlrev_b32_e32 v3, 3, v2
	global_load_lds_dwordx4 v1, s[20:21]
	v_and_b32_e32 v1, 15, v0
	v_lshlrev_b32_e32 v2, 4, v2
	v_lshlrev_b32_e32 v0, 2, v0
	v_lshl_or_b32 v212, s40, 6, v1
	v_lshl_or_b32 v1, v1, 6, v2
	v_and_b32_e32 v0, 32, v0
	s_waitcnt vmcnt(6)
	v_bitop3_b32 v2, v1, s41, v0 bitop3:0xde
	s_cmpk_lt_u32 s29, 0x100
	v_bitop3_b32 v213, v1, s43, v0 bitop3:0xde
	s_cselect_b64 s[40:41], -1, 0
	v_lshl_or_b32 v214, s42, 5, v3
	v_or_b32_e32 v215, 16, v212
	v_or_b32_e32 v219, 32, v212
	v_or_b32_e32 v220, 48, v212
	s_mov_b32 s59, 0
	v_add_u32_e32 v221, 0, v2
	s_mov_b64 s[46:47], s[4:5]
	s_mov_b64 s[44:45], s[2:3]
	s_barrier
	s_waitcnt vmcnt(0)
	s_branch .LBB0_1259

; template <class Desc, class Epi>
; __device__ __forceinline__ void gemm_phase(const int wv_, LAS unsigned char* lds, const Desc& d, const Epi& E) {
;     ...
; #pragma unroll
;         for (int a = 0; a < 2; ++a)
; #pragma unroll
;             for (int b = 0; b < 2; ++b)
; #pragma unroll
;                 for (int m = 0; m < 4; ++m)
; #pragma unroll
;                     for (int n = 0; n < 2; ++n) acc[a][b][m][n] = (f32x4){0.f, 0.f, 0.f, 0.f};
;         cur = nxt; cA = nA; cB = nB; ++ui;
;         if constexpr (Desc::GATHER) { voffA[0] = voffAn[0]; voffA[1] = voffAn[1]; voffA1[0] = voffAn1[0]; voffA1[1] = voffAn1[1]; }
.LBB0_1261:
	s_add_u32 s2, s2, 0x80
	s_addc_u32 s3, s3, 0
	s_add_u32 s29, s4, 0x100
	v_mov_b32_e32 v20, 0
	s_addc_u32 s43, s5, 0
	s_mov_b32 s61, -2
	v_mov_b32_e32 v21, v20
	v_mov_b32_e32 v22, v20
	v_mov_b32_e32 v23, v20
	v_mov_b32_e32 v28, v20
	v_mov_b32_e32 v29, v20
	v_mov_b32_e32 v30, v20
	v_mov_b32_e32 v31, v20
	v_mov_b32_e32 v48, v20
	v_mov_b32_e32 v49, v20
	v_mov_b32_e32 v50, v20
	v_mov_b32_e32 v51, v20
	v_mov_b32_e32 v52, v20
	v_mov_b32_e32 v53, v20
	v_mov_b32_e32 v54, v20
	v_mov_b32_e32 v55, v20
	v_mov_b32_e32 v0, v20
	v_mov_b32_e32 v1, v20
	v_mov_b32_e32 v2, v20
	v_mov_b32_e32 v3, v20
	v_mov_b32_e32 v4, v20
	v_mov_b32_e32 v5, v20
	v_mov_b32_e32 v6, v20
	v_mov_b32_e32 v7, v20
	v_mov_b32_e32 v16, v20
	v_mov_b32_e32 v17, v20
	v_mov_b32_e32 v18, v20
	v_mov_b32_e32 v19, v20
	v_mov_b32_e32 v24, v20
	v_mov_b32_e32 v25, v20
	v_mov_b32_e32 v26, v20
	v_mov_b32_e32 v27, v20
	v_mov_b32_e32 v40, v20
	v_mov_b32_e32 v41, v20
	v_mov_b32_e32 v42, v20
	v_mov_b32_e32 v43, v20
	v_mov_b32_e32 v44, v20
	v_mov_b32_e32 v45, v20
	v_mov_b32_e32 v46, v20
	v_mov_b32_e32 v47, v20
	v_mov_b32_e32 v56, v20
	v_mov_b32_e32 v57, v20
	v_mov_b32_e32 v58, v20
	v_mov_b32_e32 v59, v20
	v_mov_b32_e32 v60, v20
	v_mov_b32_e32 v61, v20
	v_mov_b32_e32 v62, v20
	v_mov_b32_e32 v63, v20
	v_mov_b32_e32 v64, v20
	v_mov_b32_e32 v65, v20
	v_mov_b32_e32 v66, v20
	v_mov_b32_e32 v67, v20
	v_mov_b32_e32 v68, v20
	v_mov_b32_e32 v69, v20
	v_mov_b32_e32 v70, v20
	v_mov_b32_e32 v71, v20
	v_mov_b32_e32 v80, v20
	v_mov_b32_e32 v81, v20
	v_mov_b32_e32 v82, v20
	v_mov_b32_e32 v83, v20
	v_mov_b32_e32 v84, v20
	v_mov_b32_e32 v85, v20
	v_mov_b32_e32 v86, v20
	v_mov_b32_e32 v87, v20
	v_mov_b32_e32 v98, v20
	v_mov_b32_e32 v99, v20
	v_mov_b32_e32 v100, v20
	v_mov_b32_e32 v101, v20
	v_mov_b32_e32 v102, v20
	v_mov_b32_e32 v103, v20
	v_mov_b32_e32 v104, v20
	v_mov_b32_e32 v105, v20
	v_mov_b32_e32 v114, v20
	v_mov_b32_e32 v115, v20
	v_mov_b32_e32 v116, v20
	v_mov_b32_e32 v117, v20
	v_mov_b32_e32 v118, v20
	v_mov_b32_e32 v119, v20
	v_mov_b32_e32 v120, v20
	v_mov_b32_e32 v121, v20
	v_mov_b32_e32 v72, v20
	v_mov_b32_e32 v73, v20
	v_mov_b32_e32 v74, v20
	v_mov_b32_e32 v75, v20
	v_mov_b32_e32 v76, v20
	v_mov_b32_e32 v77, v20
	v_mov_b32_e32 v78, v20
	v_mov_b32_e32 v79, v20
	v_mov_b32_e32 v88, v20
	v_mov_b32_e32 v89, v20
	v_mov_b32_e32 v90, v20
	v_mov_b32_e32 v91, v20
	v_mov_b32_e32 v92, v20
	v_mov_b32_e32 v93, v20
	v_mov_b32_e32 v94, v20
	v_mov_b32_e32 v95, v20
	v_mov_b32_e32 v106, v20
	v_mov_b32_e32 v107, v20
	v_mov_b32_e32 v108, v20
	v_mov_b32_e32 v109, v20
	v_mov_b32_e32 v110, v20
	v_mov_b32_e32 v111, v20
	v_mov_b32_e32 v112, v20
	v_mov_b32_e32 v113, v20
	v_mov_b32_e32 v122, v20
	v_mov_b32_e32 v123, v20
	v_mov_b32_e32 v124, v20
	v_mov_b32_e32 v125, v20
	v_mov_b32_e32 v126, v20
	v_mov_b32_e32 v127, v20
	v_mov_b32_e32 v128, v20
	v_mov_b32_e32 v129, v20
	v_mov_b32_e32 v36, v20
	v_mov_b32_e32 v37, v20
	v_mov_b32_e32 v38, v20
	v_mov_b32_e32 v39, v20
	v_mov_b32_e32 v32, v20
	v_mov_b32_e32 v33, v20
	v_mov_b32_e32 v34, v20
	v_mov_b32_e32 v35, v20
	v_mov_b32_e32 v12, v20
	v_mov_b32_e32 v13, v20
	v_mov_b32_e32 v14, v20
	v_mov_b32_e32 v15, v20
	v_mov_b32_e32 v8, v20
	v_mov_b32_e32 v9, v20
	v_mov_b32_e32 v10, v20
	v_mov_b32_e32 v11, v20

; #define PG8_STAGE(bufoff, gbase, voff) do { _Pragma("unroll") for (int _i = 0; _i < 2; ++_i) \
;         __builtin_amdgcn_global_load_lds((const __attribute__((address_space(1))) unsigned*)((const __attribute__((address_space(1))) char*)(gbase) + (unsigned)lnd_v((int)(voff)[_i])), (LAS unsigned*)(lds + (bufoff) + ldsw + _i * 8192), 16, 0, 0); } while (0)
; #define PG8_WAIT_V(n) asm volatile("s_waitcnt vmcnt(" #n ")" ::: "memory")
; #define PG8_BAR __builtin_amdgcn_s_barrier()
; template <class Desc, class Epi>
; __device__ __forceinline__ void gemm_phase(const int wv_, LAS unsigned char* lds, const Desc& d, const Epi& E) {
;     ...
;     const unsigned ldsw = (unsigned)wid * 1024u;
;     const int aoff = lds_byte(wr * 64 + fr, fq * 8), boff = lds_byte(wc * 32 + fr, fq * 8);
;     ...
;     const char* cA = (const char*)cur.a; const char* cB = (const char*)cur.b;
;     PG8_STAGE(PG8_SB(0, 0), cB, voffB); PG8_STAGE(PG8_SB(0, 1), cB + hstepB, voffB); PG8_STAGE(PG8_SA(0, 0), cA, voffA); PG8_STAGE(PG8_SA(0, 1), cA, voffA1);
;     if (wr == 1) PG8_BAR;
;     PG8_WAIT_V(2); PG8_BAR;
;     PG8_STAGE(PG8_SB(1, 0), cB + kstep, voffB); PG8_STAGE(PG8_SA(1, 0), cA + kstep, voffA); PG8_STAGE(PG8_SB(1, 1), cB + hstepB + kstep, voffB);
;     PG8_WAIT_V(6); PG8_BAR;
.LBB0_1475:
	s_lshl_b32 s23, s26, 5
	s_lshl_b32 s1, s1, 2
	s_or_b32 s1, s1, s23
	s_or_b32 s1, s1, s22
	v_mov_b32_e32 v96, v134
	s_add_u32 s38, s2, 0x3f200000
	s_waitcnt vmcnt(2)
	s_barrier
	s_addc_u32 s39, s3, 0
	v_lshl_add_u64 v[2:3], s[48:49], 0, v[96:97]
	s_add_i32 m0, s60, 0x18000
	v_lshl_add_u64 v[2:3], v[2:3], 0, s[30:31]
	v_mov_b32_e32 v96, v137
	global_load_lds_dwordx4 v[2:3], off
	s_lshl_b32 s2, s5, 5
	v_lshl_add_u64 v[2:3], s[48:49], 0, v[96:97]
	v_lshl_add_u64 v[2:3], v[2:3], 0, s[30:31]
	s_add_i32 m0, s60, 0x1a000
	v_mov_b32_e32 v96, v132
	s_and_b32 s5, s2, 0x60
	v_readlane_b32 s2, v254, 57
	global_load_lds_dwordx4 v[2:3], off
	s_add_i32 s65, s60, 0x8000
	v_lshl_add_u64 v[2:3], s[50:51], 0, v[96:97]
	s_lshl_b32 s64, s2, 7
	v_lshl_add_u64 v[2:3], v[2:3], 0, s[30:31]
	s_mov_b32 m0, s65
	v_mov_b32_e32 v96, v135
	s_add_i32 s26, s21, 0xffffff80
	s_lshl_b32 s21, s4, 13
	s_lshl_b32 s22, s5, 7
	s_addk_i32 s64, 0x80
	global_load_lds_dwordx4 v[2:3], off
	s_add_i32 s66, s60, 0xa000
	v_lshl_add_u64 v[2:3], s[50:51], 0, v[96:97]
	v_readlane_b32 s3, v254, 58
	v_lshl_add_u64 v[2:3], v[2:3], 0, s[30:31]
	s_mov_b32 m0, s66
	s_add_u32 s2, s48, 0x40080
	v_mov_b32_e32 v1, v134
	global_load_lds_dwordx4 v[2:3], off
	s_addc_u32 s3, s49, 0
	s_add_i32 m0, s60, 0x1c000
	v_lshrrev_b32_e32 v2, 1, v0
	global_load_lds_dwordx4 v1, s[2:3]
	v_mov_b32_e32 v1, v137
	s_add_i32 m0, s60, 0x1e000
	v_and_b32_e32 v2, 24, v2
	global_load_lds_dwordx4 v1, s[2:3]
	v_and_b32_e32 v1, 15, v0
	v_lshl_or_b32 v138, s4, 6, v1
	v_lshlrev_b32_e32 v3, 1, v2
	v_lshl_or_b32 v1, v1, 6, v3
	v_lshlrev_b32_e32 v3, 2, v138
	v_and_b32_e32 v4, 32, v3
	v_lshlrev_b32_e32 v0, 2, v0
	s_waitcnt vmcnt(6)
	s_cmpk_lt_u32 s20, 0x100
	v_bitop3_b32 v4, v1, s21, v4 bitop3:0xde
	v_and_b32_e32 v0, 32, v0
	s_cselect_b64 s[40:41], -1, 0
	s_add_i32 s2, 0, 0x20000
	v_bitop3_b32 v139, v1, s22, v0 bitop3:0xde
	v_or_b32_e32 v140, 16, v138
	v_or_b32_e32 v141, 32, v138
	v_or_b32_e32 v142, 48, v138
	v_add_u32_e32 v143, 0x80, v138
	v_add_u32_e32 v144, 0x90, v138
	v_add_u32_e32 v145, 0xa0, v138
	v_add_u32_e32 v146, 0xb0, v138
	v_or_b32_e32 v147, s5, v2
	v_add_u32_e32 v148, s2, v3
	s_mov_b32 s70, 0
	v_add_u32_e32 v149, 0, v4
	s_mov_b64 s[44:45], s[48:49]
	s_mov_b64 s[42:43], s[50:51]
	s_barrier
	s_waitcnt vmcnt(0)
	s_branch .LBB0_1478

; #define PG8_AOFF(ord, U, O0, O1) do { _Pragma("unroll") for (int _i = 0; _i < 2; ++_i) { \
;         O0[_i] = d.rowbyte(U, (int)tix[(ord) * 256 + Rr[_i]]) + (unsigned)(Cc[_i] * 2); O1[_i] = d.rowbyte(U, (int)tix[(ord) * 256 + HALF + Rr[_i]]) + (unsigned)(Cc[_i] * 2); } } while (0)
; #define PG8_STAGE(bufoff, gbase, voff) do { _Pragma("unroll") for (int _i = 0; _i < 2; ++_i) \
;         __builtin_amdgcn_global_load_lds((const __attribute__((address_space(1))) unsigned*)((const __attribute__((address_space(1))) char*)(gbase) + (unsigned)lnd_v((int)(voff)[_i])), (LAS unsigned*)(lds + (bufoff) + ldsw + _i * 8192), 16, 0, 0); } while (0)
; #define PG8_WAIT_V(n) asm volatile("s_waitcnt vmcnt(" #n ")" ::: "memory")
; #define PG8_BAR __builtin_amdgcn_s_barrier()
; template <class Desc, class Epi>
; __device__ __forceinline__ void gemm_phase(const int wv_, LAS unsigned char* lds, const Desc& d, const Epi& E) {
;     ...
;     if constexpr (Desc::GATHER) PG8_AOFF(0, cur, voffA, voffA1);
;     ...
;     const char* cA = (const char*)cur.a; const char* cB = (const char*)cur.b;
;     PG8_STAGE(PG8_SB(0, 0), cB, voffB); PG8_STAGE(PG8_SB(0, 1), cB + hstepB, voffB); PG8_STAGE(PG8_SA(0, 0), cA, voffA); PG8_STAGE(PG8_SA(0, 1), cA, voffA1);
;     if (wr == 1) PG8_BAR;
;     PG8_WAIT_V(2); PG8_BAR;
;     PG8_STAGE(PG8_SB(1, 0), cB + kstep, voffB); PG8_STAGE(PG8_SA(1, 0), cA + kstep, voffA); PG8_STAGE(PG8_SB(1, 1), cB + hstepB + kstep, voffB);
;     PG8_WAIT_V(6); PG8_BAR;
.LBB0_1559:
	v_mov_b32_e32 v96, v138
	s_lshl_b32 s5, s5, 5
	s_waitcnt vmcnt(2)
	s_barrier
	s_and_b32 s0, s0, 1
	v_lshl_add_u64 v[0:1], s[2:3], 0, v[96:97]
	s_and_b32 s5, s5, 0x60
	s_add_i32 m0, s64, 0x18000
	v_lshl_add_u64 v[0:1], v[0:1], 0, s[30:31]
	v_mov_b32_e32 v96, v141
	s_or_b32 s0, s20, s0
	s_lshl_b32 s22, s4, 13
	s_lshl_b32 s23, s5, 7
	global_load_lds_dwordx4 v[0:1], off
	s_add_i32 m0, s64, 0x1a000
	v_lshl_add_u64 v[0:1], s[2:3], 0, v[96:97]
	v_lshl_add_u64 v[0:1], v[0:1], 0, s[30:31]
	s_add_u32 s40, s46, 0x33600080
	global_load_lds_dwordx4 v[0:1], off
	s_addc_u32 s41, s47, 0
	v_mov_b32_e32 v0, v157
	s_add_i32 s70, s64, 0x8000
	s_mov_b32 m0, s70
	s_add_i32 s71, s64, 0xa000
	global_load_lds_dwordx4 v0, s[40:41]
	v_mov_b32_e32 v0, v159
	s_mov_b32 m0, s71
	s_add_u32 s20, s2, 0x40080
	global_load_lds_dwordx4 v0, s[40:41]
	v_mov_b32_e32 v0, v138
	s_addc_u32 s21, s3, 0
	s_add_i32 m0, s64, 0x1c000
	v_and_b32_e32 v1, 15, v4
	global_load_lds_dwordx4 v0, s[20:21]
	v_mov_b32_e32 v0, v141
	s_add_i32 m0, s64, 0x1e000
	v_lshl_or_b32 v142, s4, 6, v1
	global_load_lds_dwordx4 v0, s[20:21]
	v_lshrrev_b32_e32 v0, 1, v4
	v_and_b32_e32 v0, 24, v0
	v_lshlrev_b32_e32 v2, 1, v0
	v_lshl_or_b32 v1, v1, 6, v2
	v_lshlrev_b32_e32 v2, 2, v142
	v_and_b32_e32 v3, 32, v2
	v_lshlrev_b32_e32 v4, 2, v4
	s_waitcnt vmcnt(6)
	s_cmpk_lt_u32 s52, 0x100
	v_bitop3_b32 v3, v1, s22, v3 bitop3:0xde
	v_and_b32_e32 v4, 32, v4
	s_cselect_b64 s[52:53], -1, 0
	s_add_i32 s4, 0, 0x20000
	v_bitop3_b32 v143, v1, s23, v4 bitop3:0xde
	v_or_b32_e32 v144, 16, v142
	v_or_b32_e32 v145, 32, v142
	v_or_b32_e32 v146, 48, v142
	v_add_u32_e32 v147, 0x80, v142
	v_add_u32_e32 v148, 0x90, v142
	v_add_u32_e32 v149, 0xa0, v142
	v_add_u32_e32 v150, 0xb0, v142
	v_add_u32_e32 v151, s4, v2
	s_mov_b32 s58, 0
	v_add_u32_e32 v152, 0, v3
	s_lshl_b32 s26, s5, 1
	v_lshlrev_b32_e32 v130, 1, v0
	v_mov_b32_e32 v154, v159
	v_mov_b32_e32 v153, v157
	v_mov_b32_e32 v156, v158
	v_mov_b32_e32 v155, v131
	s_mov_b64 s[54:55], s[2:3]
	s_barrier
	s_waitcnt vmcnt(0)
	s_branch .LBB0_1562

; template <class Desc, class Epi>
; __device__ __forceinline__ void gemm_phase(const int wv_, LAS unsigned char* lds, const Desc& d, const Epi& E) {
;     ...
; #pragma unroll
;         for (int a = 0; a < 2; ++a)
; #pragma unroll
;             for (int b = 0; b < 2; ++b)
; #pragma unroll
;                 for (int m = 0; m < 4; ++m)
; #pragma unroll
;                     for (int n = 0; n < 2; ++n) acc[a][b][m][n] = (f32x4){0.f, 0.f, 0.f, 0.f};
;         cur = nxt; cA = nA; cB = nB; ++ui;
;         if constexpr (Desc::GATHER) { voffA[0] = voffAn[0]; voffA[1] = voffAn[1]; voffA1[0] = voffAn1[0]; voffA1[1] = voffAn1[1]; }
.LBB0_1564:
	s_add_u32 s29, s2, 0x100
	v_mov_b32_e32 v0, 0
	s_addc_u32 s59, s3, 0
	s_mov_b32 s75, -2
	s_mov_b64 s[2:3], 0
	v_mov_b32_e32 v1, v0
	v_mov_b32_e32 v2, v0
	v_mov_b32_e32 v3, v0
	v_mov_b32_e32 v12, v0
	v_mov_b32_e32 v13, v0
	v_mov_b32_e32 v14, v0
	v_mov_b32_e32 v15, v0
	v_mov_b32_e32 v20, v0
	v_mov_b32_e32 v21, v0
	v_mov_b32_e32 v22, v0
	v_mov_b32_e32 v23, v0
	v_mov_b32_e32 v28, v0
	v_mov_b32_e32 v29, v0
	v_mov_b32_e32 v30, v0
	v_mov_b32_e32 v31, v0
	v_mov_b32_e32 v36, v0
	v_mov_b32_e32 v37, v0
	v_mov_b32_e32 v38, v0
	v_mov_b32_e32 v39, v0
	v_mov_b32_e32 v44, v0
	v_mov_b32_e32 v45, v0
	v_mov_b32_e32 v46, v0
	v_mov_b32_e32 v47, v0
	v_mov_b32_e32 v52, v0
	v_mov_b32_e32 v53, v0
	v_mov_b32_e32 v54, v0
	v_mov_b32_e32 v55, v0
	v_mov_b32_e32 v60, v0
	v_mov_b32_e32 v61, v0
	v_mov_b32_e32 v62, v0
	v_mov_b32_e32 v63, v0
	v_mov_b32_e32 v4, v0
	v_mov_b32_e32 v5, v0
	v_mov_b32_e32 v6, v0
	v_mov_b32_e32 v7, v0
	v_mov_b32_e32 v8, v0
	v_mov_b32_e32 v9, v0
	v_mov_b32_e32 v10, v0
	v_mov_b32_e32 v11, v0
	v_mov_b32_e32 v16, v0
	v_mov_b32_e32 v17, v0
	v_mov_b32_e32 v18, v0
	v_mov_b32_e32 v19, v0
	v_mov_b32_e32 v24, v0
	v_mov_b32_e32 v25, v0
	v_mov_b32_e32 v26, v0
	v_mov_b32_e32 v27, v0
	v_mov_b32_e32 v32, v0
	v_mov_b32_e32 v33, v0
	v_mov_b32_e32 v34, v0
	v_mov_b32_e32 v35, v0
	v_mov_b32_e32 v40, v0
	v_mov_b32_e32 v41, v0
	v_mov_b32_e32 v42, v0
	v_mov_b32_e32 v43, v0
	v_mov_b32_e32 v48, v0
	v_mov_b32_e32 v49, v0
	v_mov_b32_e32 v50, v0
	v_mov_b32_e32 v51, v0
	v_mov_b32_e32 v56, v0
	v_mov_b32_e32 v57, v0
	v_mov_b32_e32 v58, v0
	v_mov_b32_e32 v59, v0
	v_mov_b32_e32 v68, v0
	v_mov_b32_e32 v69, v0
	v_mov_b32_e32 v70, v0
	v_mov_b32_e32 v71, v0
	v_mov_b32_e32 v76, v0
	v_mov_b32_e32 v77, v0
	v_mov_b32_e32 v78, v0
	v_mov_b32_e32 v79, v0
	v_mov_b32_e32 v84, v0
	v_mov_b32_e32 v85, v0
	v_mov_b32_e32 v86, v0
	v_mov_b32_e32 v87, v0
	v_mov_b32_e32 v92, v0
	v_mov_b32_e32 v93, v0
	v_mov_b32_e32 v94, v0
	v_mov_b32_e32 v95, v0
	v_mov_b32_e32 v102, v0
	v_mov_b32_e32 v103, v0
	v_mov_b32_e32 v104, v0
	v_mov_b32_e32 v105, v0
	v_mov_b32_e32 v110, v0
	v_mov_b32_e32 v111, v0
	v_mov_b32_e32 v112, v0
	v_mov_b32_e32 v113, v0
	v_mov_b32_e32 v118, v0
	v_mov_b32_e32 v119, v0
	v_mov_b32_e32 v120, v0
	v_mov_b32_e32 v121, v0
	v_mov_b32_e32 v126, v0
	v_mov_b32_e32 v127, v0
	v_mov_b32_e32 v128, v0
	v_mov_b32_e32 v129, v0
	v_mov_b32_e32 v64, v0
	v_mov_b32_e32 v65, v0
	v_mov_b32_e32 v66, v0
	v_mov_b32_e32 v67, v0
	v_mov_b32_e32 v72, v0
	v_mov_b32_e32 v73, v0
	v_mov_b32_e32 v74, v0
	v_mov_b32_e32 v75, v0
	v_mov_b32_e32 v80, v0
	v_mov_b32_e32 v81, v0
	v_mov_b32_e32 v82, v0
	v_mov_b32_e32 v83, v0
	v_mov_b32_e32 v88, v0
	v_mov_b32_e32 v89, v0
	v_mov_b32_e32 v90, v0
	v_mov_b32_e32 v91, v0
	v_mov_b32_e32 v98, v0
	v_mov_b32_e32 v99, v0
	v_mov_b32_e32 v100, v0
	v_mov_b32_e32 v101, v0
	v_mov_b32_e32 v106, v0
	v_mov_b32_e32 v107, v0
	v_mov_b32_e32 v108, v0
	v_mov_b32_e32 v109, v0
	v_mov_b32_e32 v114, v0
	v_mov_b32_e32 v115, v0
	v_mov_b32_e32 v116, v0
	v_mov_b32_e32 v117, v0
	v_mov_b32_e32 v122, v0
	v_mov_b32_e32 v123, v0
	v_mov_b32_e32 v124, v0
	v_mov_b32_e32 v125, v0

; #define PG8_AOFF(ord, U, O0, O1) do { _Pragma("unroll") for (int _i = 0; _i < 2; ++_i) { \
;         O0[_i] = d.rowbyte(U, (int)tix[(ord) * 256 + Rr[_i]]) + (unsigned)(Cc[_i] * 2); O1[_i] = d.rowbyte(U, (int)tix[(ord) * 256 + HALF + Rr[_i]]) + (unsigned)(Cc[_i] * 2); } } while (0)
; #define PG8_STAGE(bufoff, gbase, voff) do { _Pragma("unroll") for (int _i = 0; _i < 2; ++_i) \
;         __builtin_amdgcn_global_load_lds((const __attribute__((address_space(1))) unsigned*)((const __attribute__((address_space(1))) char*)(gbase) + (unsigned)lnd_v((int)(voff)[_i])), (LAS unsigned*)(lds + (bufoff) + ldsw + _i * 8192), 16, 0, 0); } while (0)
; #define PG8_WAIT_V(n) asm volatile("s_waitcnt vmcnt(" #n ")" ::: "memory")
; #define PG8_BAR __builtin_amdgcn_s_barrier()
; template <class Desc, class Epi>
; __device__ __forceinline__ void gemm_phase(const int wv_, LAS unsigned char* lds, const Desc& d, const Epi& E) {
;     ...
;     if constexpr (Desc::GATHER) PG8_AOFF(0, cur, voffA, voffA1);
;     ...
;     const char* cA = (const char*)cur.a; const char* cB = (const char*)cur.b;
;     PG8_STAGE(PG8_SB(0, 0), cB, voffB); PG8_STAGE(PG8_SB(0, 1), cB + hstepB, voffB); PG8_STAGE(PG8_SA(0, 0), cA, voffA); PG8_STAGE(PG8_SA(0, 1), cA, voffA1);
;     if (wr == 1) PG8_BAR;
;     PG8_WAIT_V(2); PG8_BAR;
;     PG8_STAGE(PG8_SB(1, 0), cB + kstep, voffB); PG8_STAGE(PG8_SA(1, 0), cA + kstep, voffA); PG8_STAGE(PG8_SB(1, 1), cB + hstepB + kstep, voffB);
;     PG8_WAIT_V(6); PG8_BAR;
.LBB0_1855:
	v_mov_b32_e32 v96, v138
	s_lshl_b32 s5, s5, 5
	s_waitcnt vmcnt(2)
	s_barrier
	s_and_b32 s0, s0, 1
	v_lshl_add_u64 v[0:1], s[2:3], 0, v[96:97]
	s_and_b32 s5, s5, 0x60
	s_add_i32 m0, s57, 0x18000
	v_lshl_add_u64 v[0:1], v[0:1], 0, s[30:31]
	v_mov_b32_e32 v96, v141
	s_or_b32 s0, s20, s0
	s_lshl_b32 s22, s4, 13
	s_lshl_b32 s23, s5, 7
	global_load_lds_dwordx4 v[0:1], off
	s_add_i32 m0, s57, 0x1a000
	v_lshl_add_u64 v[0:1], s[2:3], 0, v[96:97]
	v_lshl_add_u64 v[0:1], v[0:1], 0, s[30:31]
	s_add_u32 s38, s46, 0x33600080
	global_load_lds_dwordx4 v[0:1], off
	s_addc_u32 s39, s47, 0
	v_mov_b32_e32 v0, v157
	s_add_i32 s61, s57, 0x8000
	s_mov_b32 m0, s61
	s_add_i32 s62, s57, 0xa000
	global_load_lds_dwordx4 v0, s[38:39]
	v_mov_b32_e32 v0, v159
	s_mov_b32 m0, s62
	s_add_u32 s20, s2, 0x40080
	global_load_lds_dwordx4 v0, s[38:39]
	v_mov_b32_e32 v0, v138
	s_addc_u32 s21, s3, 0
	s_add_i32 m0, s57, 0x1c000
	v_and_b32_e32 v1, 15, v4
	global_load_lds_dwordx4 v0, s[20:21]
	v_mov_b32_e32 v0, v141
	s_add_i32 m0, s57, 0x1e000
	v_lshl_or_b32 v142, s4, 6, v1
	global_load_lds_dwordx4 v0, s[20:21]
	v_lshrrev_b32_e32 v0, 1, v4
	v_and_b32_e32 v0, 24, v0
	v_lshlrev_b32_e32 v2, 1, v0
	v_lshl_or_b32 v1, v1, 6, v2
	v_lshlrev_b32_e32 v2, 2, v142
	v_and_b32_e32 v3, 32, v2
	v_lshlrev_b32_e32 v4, 2, v4
	s_waitcnt vmcnt(6)
	s_cmpk_lt_u32 s40, 0x100
	v_bitop3_b32 v3, v1, s22, v3 bitop3:0xde
	v_and_b32_e32 v4, 32, v4
	s_cselect_b64 s[40:41], -1, 0
	s_add_i32 s4, 0, 0x20000
	v_bitop3_b32 v143, v1, s23, v4 bitop3:0xde
	v_or_b32_e32 v144, 16, v142
	v_or_b32_e32 v145, 32, v142
	v_or_b32_e32 v146, 48, v142
	v_add_u32_e32 v147, 0x80, v142
	v_add_u32_e32 v148, 0x90, v142
	v_add_u32_e32 v149, 0xa0, v142
	v_add_u32_e32 v150, 0xb0, v142
	v_add_u32_e32 v151, s4, v2
	s_mov_b32 s50, 0
	v_add_u32_e32 v152, 0, v3
	s_lshl_b32 s26, s5, 1
	v_lshlrev_b32_e32 v130, 1, v0
	v_mov_b32_e32 v154, v159
	v_mov_b32_e32 v153, v157
	v_mov_b32_e32 v156, v158
	v_mov_b32_e32 v155, v131
	s_mov_b64 s[46:47], s[2:3]
	s_barrier
	s_waitcnt vmcnt(0)
	s_branch .LBB0_1858

; template <class Desc, class Epi>
; __device__ __forceinline__ void gemm_phase(const int wv_, LAS unsigned char* lds, const Desc& d, const Epi& E) {
;     ...
; #pragma unroll
;         for (int a = 0; a < 2; ++a)
; #pragma unroll
;             for (int b = 0; b < 2; ++b)
; #pragma unroll
;                 for (int m = 0; m < 4; ++m)
; #pragma unroll
;                     for (int n = 0; n < 2; ++n) acc[a][b][m][n] = (f32x4){0.f, 0.f, 0.f, 0.f};
;         cur = nxt; cA = nA; cB = nB; ++ui;
;         if constexpr (Desc::GATHER) { voffA[0] = voffAn[0]; voffA[1] = voffAn[1]; voffA1[0] = voffAn1[0]; voffA1[1] = voffAn1[1]; }
.LBB0_1860:
	s_add_u32 s29, s2, 0x100
	v_mov_b32_e32 v0, 0
	s_addc_u32 s51, s3, 0
	s_mov_b32 s66, -2
	s_mov_b64 s[2:3], 0
	v_mov_b32_e32 v1, v0
	v_mov_b32_e32 v2, v0
	v_mov_b32_e32 v3, v0
	v_mov_b32_e32 v12, v0
	v_mov_b32_e32 v13, v0
	v_mov_b32_e32 v14, v0
	v_mov_b32_e32 v15, v0
	v_mov_b32_e32 v20, v0
	v_mov_b32_e32 v21, v0
	v_mov_b32_e32 v22, v0
	v_mov_b32_e32 v23, v0
	v_mov_b32_e32 v28, v0
	v_mov_b32_e32 v29, v0
	v_mov_b32_e32 v30, v0
	v_mov_b32_e32 v31, v0
	v_mov_b32_e32 v36, v0
	v_mov_b32_e32 v37, v0
	v_mov_b32_e32 v38, v0
	v_mov_b32_e32 v39, v0
	v_mov_b32_e32 v44, v0
	v_mov_b32_e32 v45, v0
	v_mov_b32_e32 v46, v0
	v_mov_b32_e32 v47, v0
	v_mov_b32_e32 v52, v0
	v_mov_b32_e32 v53, v0
	v_mov_b32_e32 v54, v0
	v_mov_b32_e32 v55, v0
	v_mov_b32_e32 v60, v0
	v_mov_b32_e32 v61, v0
	v_mov_b32_e32 v62, v0
	v_mov_b32_e32 v63, v0
	v_mov_b32_e32 v4, v0
	v_mov_b32_e32 v5, v0
	v_mov_b32_e32 v6, v0
	v_mov_b32_e32 v7, v0
	v_mov_b32_e32 v8, v0
	v_mov_b32_e32 v9, v0
	v_mov_b32_e32 v10, v0
	v_mov_b32_e32 v11, v0
	v_mov_b32_e32 v16, v0
	v_mov_b32_e32 v17, v0
	v_mov_b32_e32 v18, v0
	v_mov_b32_e32 v19, v0
	v_mov_b32_e32 v24, v0
	v_mov_b32_e32 v25, v0
	v_mov_b32_e32 v26, v0
	v_mov_b32_e32 v27, v0
	v_mov_b32_e32 v32, v0
	v_mov_b32_e32 v33, v0
	v_mov_b32_e32 v34, v0
	v_mov_b32_e32 v35, v0
	v_mov_b32_e32 v40, v0
	v_mov_b32_e32 v41, v0
	v_mov_b32_e32 v42, v0
	v_mov_b32_e32 v43, v0
	v_mov_b32_e32 v48, v0
	v_mov_b32_e32 v49, v0
	v_mov_b32_e32 v50, v0
	v_mov_b32_e32 v51, v0
	v_mov_b32_e32 v56, v0
	v_mov_b32_e32 v57, v0
	v_mov_b32_e32 v58, v0
	v_mov_b32_e32 v59, v0
	v_mov_b32_e32 v68, v0
	v_mov_b32_e32 v69, v0
	v_mov_b32_e32 v70, v0
	v_mov_b32_e32 v71, v0
	v_mov_b32_e32 v76, v0
	v_mov_b32_e32 v77, v0
	v_mov_b32_e32 v78, v0
	v_mov_b32_e32 v79, v0
	v_mov_b32_e32 v84, v0
	v_mov_b32_e32 v85, v0
	v_mov_b32_e32 v86, v0
	v_mov_b32_e32 v87, v0
	v_mov_b32_e32 v92, v0
	v_mov_b32_e32 v93, v0
	v_mov_b32_e32 v94, v0
	v_mov_b32_e32 v95, v0
	v_mov_b32_e32 v102, v0
	v_mov_b32_e32 v103, v0
	v_mov_b32_e32 v104, v0
	v_mov_b32_e32 v105, v0
	v_mov_b32_e32 v110, v0
	v_mov_b32_e32 v111, v0
	v_mov_b32_e32 v112, v0
	v_mov_b32_e32 v113, v0
	v_mov_b32_e32 v118, v0
	v_mov_b32_e32 v119, v0
	v_mov_b32_e32 v120, v0
	v_mov_b32_e32 v121, v0
	v_mov_b32_e32 v126, v0
	v_mov_b32_e32 v127, v0
	v_mov_b32_e32 v128, v0
	v_mov_b32_e32 v129, v0
	v_mov_b32_e32 v64, v0
	v_mov_b32_e32 v65, v0
	v_mov_b32_e32 v66, v0
	v_mov_b32_e32 v67, v0
	v_mov_b32_e32 v72, v0
	v_mov_b32_e32 v73, v0
	v_mov_b32_e32 v74, v0
	v_mov_b32_e32 v75, v0
	v_mov_b32_e32 v80, v0
	v_mov_b32_e32 v81, v0
	v_mov_b32_e32 v82, v0
	v_mov_b32_e32 v83, v0
	v_mov_b32_e32 v88, v0
	v_mov_b32_e32 v89, v0
	v_mov_b32_e32 v90, v0
	v_mov_b32_e32 v91, v0
	v_mov_b32_e32 v98, v0
	v_mov_b32_e32 v99, v0
	v_mov_b32_e32 v100, v0
	v_mov_b32_e32 v101, v0
	v_mov_b32_e32 v106, v0
	v_mov_b32_e32 v107, v0
	v_mov_b32_e32 v108, v0
	v_mov_b32_e32 v109, v0
	v_mov_b32_e32 v114, v0
	v_mov_b32_e32 v115, v0
	v_mov_b32_e32 v116, v0
	v_mov_b32_e32 v117, v0
	v_mov_b32_e32 v122, v0
	v_mov_b32_e32 v123, v0
	v_mov_b32_e32 v124, v0
	v_mov_b32_e32 v125, v0

; #define PG8_STAGE(bufoff, gbase, voff) do { _Pragma("unroll") for (int _i = 0; _i < 2; ++_i) \
;         __builtin_amdgcn_global_load_lds((const __attribute__((address_space(1))) unsigned*)((const __attribute__((address_space(1))) char*)(gbase) + (unsigned)lnd_v((int)(voff)[_i])), (LAS unsigned*)(lds + (bufoff) + ldsw + _i * 8192), 16, 0, 0); } while (0)
; #define PG8_WAIT_V(n) asm volatile("s_waitcnt vmcnt(" #n ")" ::: "memory")
; #define PG8_BAR __builtin_amdgcn_s_barrier()
; template <class Desc, class Epi>
; __device__ __forceinline__ void gemm_phase(const int wv_, LAS unsigned char* lds, const Desc& d, const Epi& E) {
;     ...
;     const unsigned ldsw = (unsigned)wid * 1024u;
;     const int aoff = lds_byte(wr * 64 + fr, fq * 8), boff = lds_byte(wc * 32 + fr, fq * 8);
;     ...
;     const char* cA = (const char*)cur.a; const char* cB = (const char*)cur.b;
;     PG8_STAGE(PG8_SB(0, 0), cB, voffB); PG8_STAGE(PG8_SB(0, 1), cB + hstepB, voffB); PG8_STAGE(PG8_SA(0, 0), cA, voffA); PG8_STAGE(PG8_SA(0, 1), cA, voffA1);
;     if (wr == 1) PG8_BAR;
;     PG8_WAIT_V(2); PG8_BAR;
;     PG8_STAGE(PG8_SB(1, 0), cB + kstep, voffB); PG8_STAGE(PG8_SA(1, 0), cA + kstep, voffA); PG8_STAGE(PG8_SB(1, 1), cB + hstepB + kstep, voffB);
;     PG8_WAIT_V(6); PG8_BAR;
.LBB0_1936:
	v_mov_b32_e32 v96, v134
	s_add_u32 s38, s2, 0x5b800000
	s_waitcnt vmcnt(2)
	s_barrier
	s_addc_u32 s39, s29, 0
	v_lshl_add_u64 v[0:1], s[4:5], 0, v[96:97]
	s_add_i32 m0, s53, 0x18000
	v_lshl_add_u64 v[0:1], v[0:1], 0, s[30:31]
	v_mov_b32_e32 v96, v137
	global_load_lds_dwordx4 v[0:1], off
	s_add_i32 m0, s53, 0x1a000
	v_lshl_add_u64 v[0:1], s[4:5], 0, v[96:97]
	v_lshl_add_u64 v[0:1], v[0:1], 0, s[30:31]
	v_mov_b32_e32 v96, v132
	global_load_lds_dwordx4 v[0:1], off
	s_add_i32 s57, s53, 0x8000
	v_lshl_add_u64 v[0:1], s[20:21], 0, v[96:97]
	s_lshl_b32 s29, s41, 5
	v_lshl_add_u64 v[0:1], v[0:1], 0, s[30:31]
	s_mov_b32 m0, s57
	v_mov_b32_e32 v96, v135
	s_and_b32 s29, s29, 0x60
	global_load_lds_dwordx4 v[0:1], off
	s_add_i32 s58, s53, 0xa000
	v_lshl_add_u64 v[0:1], s[20:21], 0, v[96:97]
	s_lshl_b32 s2, s40, 13
	s_lshl_b32 s41, s29, 7
	v_lshl_add_u64 v[0:1], v[0:1], 0, s[30:31]
	s_mov_b32 m0, s58
	s_add_u32 s42, s4, 0x80080
	global_load_lds_dwordx4 v[0:1], off
	v_mov_b32_e32 v0, v134
	s_addc_u32 s43, s5, 0
	s_add_i32 m0, s53, 0x1c000
	v_lshrrev_b32_e32 v1, 1, v4
	global_load_lds_dwordx4 v0, s[42:43]
	v_mov_b32_e32 v0, v137
	s_add_i32 m0, s53, 0x1e000
	v_and_b32_e32 v1, 24, v1
	global_load_lds_dwordx4 v0, s[42:43]
	v_and_b32_e32 v0, 15, v4
	v_lshl_or_b32 v138, s40, 6, v0
	v_lshlrev_b32_e32 v2, 1, v1
	v_lshl_or_b32 v0, v0, 6, v2
	v_lshlrev_b32_e32 v2, 2, v138
	v_lshlrev_b32_e32 v4, 2, v4
	v_and_b32_e32 v3, 32, v2
	v_and_b32_e32 v4, 32, v4
	s_waitcnt vmcnt(6)
	s_cmpk_lt_u32 s3, 0x100
	v_bitop3_b32 v3, v0, s2, v3 bitop3:0xde
	v_bitop3_b32 v139, v0, s41, v4 bitop3:0xde
	s_cselect_b64 s[40:41], -1, 0
	s_add_i32 s2, 0, 0x20000
	v_or_b32_e32 v140, 16, v138
	v_or_b32_e32 v141, 32, v138
	v_or_b32_e32 v142, 48, v138
	v_add_u32_e32 v143, 0x80, v138
	v_add_u32_e32 v144, 0x90, v138
	v_add_u32_e32 v145, 0xa0, v138
	v_add_u32_e32 v146, 0xb0, v138
	v_or_b32_e32 v147, s29, v1
	v_add_u32_e32 v148, s2, v2
	s_mov_b32 s61, 0
	v_add_u32_e32 v149, 0, v3
	s_mov_b64 s[44:45], s[4:5]
	s_mov_b64 s[46:47], s[20:21]
	s_barrier
	s_waitcnt vmcnt(0)
	s_branch .LBB0_1939

; template <class Desc, class Epi>
; __device__ __forceinline__ void gemm_phase(const int wv_, LAS unsigned char* lds, const Desc& d, const Epi& E) {
;     ...
; #pragma unroll
;         for (int a = 0; a < 2; ++a)
; #pragma unroll
;             for (int b = 0; b < 2; ++b)
; #pragma unroll
;                 for (int m = 0; m < 4; ++m)
; #pragma unroll
;                     for (int n = 0; n < 2; ++n) acc[a][b][m][n] = (f32x4){0.f, 0.f, 0.f, 0.f};
;         cur = nxt; cA = nA; cB = nB; ++ui;
;         if constexpr (Desc::GATHER) { voffA[0] = voffAn[0]; voffA[1] = voffAn[1]; voffA1[0] = voffAn1[0]; voffA1[1] = voffAn1[1]; }
.LBB0_1941:
	s_add_u32 s2, s20, 0x80
	s_addc_u32 s3, s21, 0
	s_add_u32 s29, s4, 0x100
	v_mov_b32_e32 v12, 0
	s_addc_u32 s43, s5, 0
	s_mov_b32 s62, -2
	v_mov_b32_e32 v13, v12
	v_mov_b32_e32 v14, v12
	v_mov_b32_e32 v15, v12
	v_mov_b32_e32 v28, v12
	v_mov_b32_e32 v29, v12
	v_mov_b32_e32 v30, v12
	v_mov_b32_e32 v31, v12
	v_mov_b32_e32 v48, v12
	v_mov_b32_e32 v49, v12
	v_mov_b32_e32 v50, v12
	v_mov_b32_e32 v51, v12
	v_mov_b32_e32 v52, v12
	v_mov_b32_e32 v53, v12
	v_mov_b32_e32 v54, v12
	v_mov_b32_e32 v55, v12
	v_mov_b32_e32 v0, v12
	v_mov_b32_e32 v1, v12
	v_mov_b32_e32 v2, v12
	v_mov_b32_e32 v3, v12
	v_mov_b32_e32 v4, v12
	v_mov_b32_e32 v5, v12
	v_mov_b32_e32 v6, v12
	v_mov_b32_e32 v7, v12
	v_mov_b32_e32 v8, v12
	v_mov_b32_e32 v9, v12
	v_mov_b32_e32 v10, v12
	v_mov_b32_e32 v11, v12
	v_mov_b32_e32 v16, v12
	v_mov_b32_e32 v17, v12
	v_mov_b32_e32 v18, v12
	v_mov_b32_e32 v19, v12
	v_mov_b32_e32 v32, v12
	v_mov_b32_e32 v33, v12
	v_mov_b32_e32 v34, v12
	v_mov_b32_e32 v35, v12
	v_mov_b32_e32 v44, v12
	v_mov_b32_e32 v45, v12
	v_mov_b32_e32 v46, v12
	v_mov_b32_e32 v47, v12
	v_mov_b32_e32 v56, v12
	v_mov_b32_e32 v57, v12
	v_mov_b32_e32 v58, v12
	v_mov_b32_e32 v59, v12
	v_mov_b32_e32 v60, v12
	v_mov_b32_e32 v61, v12
	v_mov_b32_e32 v62, v12
	v_mov_b32_e32 v63, v12
	v_mov_b32_e32 v64, v12
	v_mov_b32_e32 v65, v12
	v_mov_b32_e32 v66, v12
	v_mov_b32_e32 v67, v12
	v_mov_b32_e32 v68, v12
	v_mov_b32_e32 v69, v12
	v_mov_b32_e32 v70, v12
	v_mov_b32_e32 v71, v12
	v_mov_b32_e32 v80, v12
	v_mov_b32_e32 v81, v12
	v_mov_b32_e32 v82, v12
	v_mov_b32_e32 v83, v12
	v_mov_b32_e32 v84, v12
	v_mov_b32_e32 v85, v12
	v_mov_b32_e32 v86, v12
	v_mov_b32_e32 v87, v12
	v_mov_b32_e32 v98, v12
	v_mov_b32_e32 v99, v12
	v_mov_b32_e32 v100, v12
	v_mov_b32_e32 v101, v12
	v_mov_b32_e32 v102, v12
	v_mov_b32_e32 v103, v12
	v_mov_b32_e32 v104, v12
	v_mov_b32_e32 v105, v12
	v_mov_b32_e32 v114, v12
	v_mov_b32_e32 v115, v12
	v_mov_b32_e32 v116, v12
	v_mov_b32_e32 v117, v12
	v_mov_b32_e32 v118, v12
	v_mov_b32_e32 v119, v12
	v_mov_b32_e32 v120, v12
	v_mov_b32_e32 v121, v12
	v_mov_b32_e32 v72, v12
	v_mov_b32_e32 v73, v12
	v_mov_b32_e32 v74, v12
	v_mov_b32_e32 v75, v12
	v_mov_b32_e32 v76, v12
	v_mov_b32_e32 v77, v12
	v_mov_b32_e32 v78, v12
	v_mov_b32_e32 v79, v12
	v_mov_b32_e32 v88, v12
	v_mov_b32_e32 v89, v12
	v_mov_b32_e32 v90, v12
	v_mov_b32_e32 v91, v12
	v_mov_b32_e32 v92, v12
	v_mov_b32_e32 v93, v12
	v_mov_b32_e32 v94, v12
	v_mov_b32_e32 v95, v12
	v_mov_b32_e32 v106, v12
	v_mov_b32_e32 v107, v12
	v_mov_b32_e32 v108, v12
	v_mov_b32_e32 v109, v12
	v_mov_b32_e32 v110, v12
	v_mov_b32_e32 v111, v12
	v_mov_b32_e32 v112, v12
	v_mov_b32_e32 v113, v12
	v_mov_b32_e32 v122, v12
	v_mov_b32_e32 v123, v12
	v_mov_b32_e32 v124, v12
	v_mov_b32_e32 v125, v12
	v_mov_b32_e32 v126, v12
	v_mov_b32_e32 v127, v12
	v_mov_b32_e32 v128, v12
	v_mov_b32_e32 v129, v12
	v_mov_b32_e32 v36, v12
	v_mov_b32_e32 v37, v12
	v_mov_b32_e32 v38, v12
	v_mov_b32_e32 v39, v12
	v_mov_b32_e32 v40, v12
	v_mov_b32_e32 v41, v12
	v_mov_b32_e32 v42, v12
	v_mov_b32_e32 v43, v12
	v_mov_b32_e32 v20, v12
	v_mov_b32_e32 v21, v12
	v_mov_b32_e32 v22, v12
	v_mov_b32_e32 v23, v12
	v_mov_b32_e32 v24, v12
	v_mov_b32_e32 v25, v12
	v_mov_b32_e32 v26, v12
	v_mov_b32_e32 v27, v12
